# RWKV scan phase: hand-written recurrence loop (row-paired packed f32) + vectorized operand prep/post for waves 4-7
# speedup vs baseline: 1.0168x; 1.0168x over previous
; #define LAS __attribute__((address_space(3)))
; template <class AT_>
; __device__ __forceinline__ void rwkv_scan_phase(const AT_& a, Frame& F, int j) {
;     unsigned char* ws = a.ws; const int lane = F.lane, w = F.wave;
;     const bf16* RKV = (const bf16*)(ws + WS_BIG + 768 * MiB); const float* DEC = (const float*)(ws + WS_BIG);
;     const bf16* AG = (const bf16*)(ws + WS_BIG + 256 * MiB); const bf16* GG = (const bf16*)(ws + WS_BIG + 384 * MiB); bf16* YG = (bf16*)(ws + WS_XN);
;     const float* k_k = a.in[I_RWKK] + (size_t)j * DM; const float* k_a = a.in[I_RWKA] + (size_t)j * DM; const float* r_k = a.in[I_RWRK] + (size_t)j * DM;
;     const float* ln_w = a.in[I_RWLNW] + (size_t)j * DM; const float* ln_b = a.in[I_RWLNB] + (size_t)j * DM;
;     constexpr int OPB = 6 * RW_T * 64 * 4 + RW_T * 16;
;     LAS float* Ybase = (LAS float*)(F.lds + 2 * OPB);
;     const int vg = lane >> 3, kg = lane & 7, v0 = 16 * (w & 3) + 2 * vg;
;     for (int bh = F.bid; bh < NBATCH * RW_H; bh += F.G) {
;         const int b = bh >> 5, h = bh & 31, col = h * 64 + lane; const size_t tokb = (size_t)b * SEQ;
;         const float kkc = k_k[col], kac = k_a[col], rkc = r_k[col], lnw = ln_w[col], lnb = ln_b[col];
.LBB0_3482:
	v_readlane_b32 s0, v247, 7
	s_cmp_lt_i32 s0, 34
	s_cselect_b64 s[0:1], -1, 0
	s_cmp_gt_i32 s7, 33
	s_cselect_b64 s[2:3], -1, 0
	s_and_b64 s[0:1], s[0:1], s[2:3]
	s_andn2_b64 vcc, exec, s[0:1]
	s_cbranch_vccnz .LBB0_3567
	v_readlane_b32 s2, v247, 0
	v_readlane_b32 s3, v247, 1
	s_mov_b64 s[0:1], s[2:3]
	s_load_dword s33, s[2:3], 0x128
	s_add_u32 s12, s2, 0x128
	s_waitcnt vmcnt(0)
	v_mov_b32_e32 v2, v0
	s_addc_u32 s13, s3, 0
	s_mov_b32 s52, s76
	s_waitcnt lgkmcnt(0)
	s_mov_b32 s31, s33
	s_mov_b32 s15, 0
	s_mov_b32 s14, 0
	s_cmpk_gt_i32 s52, 0xff
	v_readfirstlane_b32 s30, v2
	s_cbranch_scc1 .LBB0_3521
	s_load_dwordx2 s[16:17], s[0:1], 0x100
	s_load_dwordx2 s[2:3], s[0:1], 0x118
	s_add_i32 s53, s14, 0
	s_ashr_i32 s54, s30, 6
	s_load_dwordx8 s[4:11], s[0:1], 0xe0
	v_lshrrev_b32_e32 v3, 2, v2
	s_waitcnt lgkmcnt(0)
	s_add_u32 s18, s2, 0x14000000
	s_addc_u32 s19, s3, 0
	s_add_u32 s20, s2, 0x44000000
	s_addc_u32 s21, s3, 0
	s_add_u32 s22, s2, 0x24000000
	s_addc_u32 s23, s3, 0
	s_add_u32 s24, s2, 0x2c000000
	s_addc_u32 s25, s3, 0
	s_add_u32 s26, s2, 0xc000000
	s_addc_u32 s27, s3, 0
	s_lshl_b32 s55, s54, 4
	s_add_i32 s0, s53, 0x18400
	v_and_b32_e32 v3, 14, v3
	s_cmp_gt_i32 s54, 3
	v_and_or_b32 v85, s55, 48, v3
	v_and_b32_e32 v3, 7, v2
	s_cselect_b64 s[28:29], -1, 0
	s_and_b32 s35, s30, 0xffffffc0
	s_and_b32 s30, s30, 0xc0
	v_and_b32_e32 v1, 63, v2
	s_add_i32 s56, s54, -4
	v_lshlrev_b32_e32 v127, 5, v3
	s_add_i32 s58, s54, 4
	s_add_i32 s60, s54, 8
	s_add_i32 s62, s54, 12
	s_add_i32 s64, s54, 16
	s_add_i32 s66, s54, 20
	s_add_i32 s68, s54, 24
	v_and_b32_e32 v2, 56, v2
	s_add_i32 s30, s14, s30
	s_lshl_b32 s34, s56, 6
	s_lshl_b32 s36, s58, 6
	s_lshl_b32 s37, s60, 6
	s_lshl_b32 s38, s62, 6
	s_lshl_b32 s39, s64, 6
	s_lshl_b32 s40, s66, 6
	s_lshl_b32 s41, s68, 6
	v_add_u32_e32 v128, s30, v2
	v_add_u32_e32 v2, s14, v127
	v_lshl_add_u32 v126, v1, 2, s0
	v_cmp_eq_u32_e64 s[0:1], 0, v1
	v_cmp_eq_u32_e64 s[2:3], 0, v3
	s_lshl_b32 s57, s56, 4
	s_lshl_b32 s59, s58, 4
	s_lshl_b32 s61, s60, 4
	s_lshl_b32 s63, s62, 4
	s_lshl_b32 s65, s64, 4
	s_lshl_b32 s67, s66, 4
	s_lshl_b32 s69, s68, 4
	s_lshl_b32 s70, s56, 8
	s_lshl_b32 s71, s54, 8
	s_lshl_b32 s72, s58, 8
	s_lshl_b32 s73, s60, 8
	s_lshl_b32 s74, s62, 8
	s_lshl_b32 s75, s64, 8
	s_lshl_b32 s76, s66, 8
	s_lshl_b32 s77, s68, 8
	s_add_i32 s78, s14, 0xc010
	v_add_u32_e32 v129, 0xa100, v128
	v_add_u32_e32 v130, 0x100, v2
	v_mov_b32_e32 v83, 0
	s_brev_b32 s79, 16
	s_brev_b32 s80, 8
	s_mov_b32 s30, 0xbfb8aa3b
	s_mov_b32 s81, 0xc200
	s_lshl_b32 s82, s34, 2
	v_mov_b32_e32 v131, 0x3a27c5ac
	s_lshl_b32 s83, s35, 2
	s_lshl_b32 s84, s36, 2
	s_lshl_b32 s85, s37, 2
	s_lshl_b32 s86, s38, 2
	s_lshl_b32 s87, s39, 2
	s_lshl_b32 s88, s40, 2
	s_lshl_b32 s89, s41, 2
	v_mov_b32_e32 v132, 0xbc800000
	v_mov_b32_e32 v133, 0x3c800000
	v_and_b32_e32 v54, 7, v1
	v_lshrrev_b32_e32 v55, 3, v1
	v_cmp_eq_u32_e64 s[100:101], 0, v54
	v_lshlrev_b32_e32 v166, 5, v54
	s_lshl_b32 s98, s54, 4
	v_lshl_add_u32 v167, v55, 1, s98
	v_lshlrev_b32_e32 v167, 2, v167
	v_and_b32_e32 v48, 7, v1
	v_lshrrev_b32_e32 v49, 3, v1
	s_lshl_b32 s78, s54, 3
	s_sub_u32 s78, s78, 32
	v_add_u32_e32 v49, s78, v49
	v_lshlrev_b32_e32 v218, 8, v49
	v_lshl_add_u32 v218, v48, 5, v218
	v_lshlrev_b32_e32 v219, 4, v49
	v_lshlrev_b32_e32 v220, 12, v49
	v_lshl_add_u32 v220, v48, 4, v220
	v_lshlrev_b32_e32 v221, 1, v220
	v_lshlrev_b32_e32 v236, 5, v48
	v_mov_b32_e32 v222, 0x3c800000
	v_mov_b32_e32 v223, 0x3a27c5ac
	v_mov_b32_e32 v120, 1.0
	v_mov_b32_e32 v121, 1.0
	s_mov_b32 s70, 0x01010101
	s_mov_b32 s71, 0x01010101
	s_mov_b32 s72, 0xbfb8aa3b
	s_mov_b32 s74, 0x3fb8aa3b
	s_mov_b32 s76, 0xbf1b4598
	s_branch .LBB0_3486

; template <class AT_>
; __device__ __forceinline__ void rwkv_scan_phase(const AT_& a, Frame& F, int j) {
;     ...
;     for (int bh = F.bid; bh < NBATCH * RW_H; bh += F.G) {
;         const int b = bh >> 5, h = bh & 31, col = h * 64 + lane; const size_t tokb = (size_t)b * SEQ;
;         const float kkc = k_k[col], kac = k_a[col], rkc = r_k[col], lnw = ln_w[col], lnb = ln_b[col];
;         f32x2 S0[4], S1[4];
; #pragma unroll
;         for (int i = 0; i < 4; ++i) { S0[i] = (f32x2){0.f, 0.f}; S1[i] = (f32x2){0.f, 0.f}; }
;     ...
;                 if (do_prep) {
; #pragma unroll
;                     for (int i = 0; i < 8; ++i) { const size_t off = (tokb + (size_t)(blk + 1) * RW_T + tw + 4 * i) * DM + col;
;                         pr[i] = bf2f(RKV[off]); pk[i] = bf2f(RKV[(size_t)MTOK * DM + off]); pv[i] = bf2f(RKV[(size_t)2 * MTOK * DM + off]); pd[i] = DEC[off]; pa[i] = bf2f(AG[off]); } }
.LBB0_3486:
	v_mov_b32_e32 v150, 0
	v_mov_b32_e32 v151, 0
	v_mov_b32_e32 v152, 0
	v_mov_b32_e32 v153, 0
	v_mov_b32_e32 v154, 0
	v_mov_b32_e32 v155, 0
	v_mov_b32_e32 v156, 0
	v_mov_b32_e32 v157, 0
	v_mov_b32_e32 v158, 0
	v_mov_b32_e32 v159, 0
	v_mov_b32_e32 v160, 0
	v_mov_b32_e32 v161, 0
	v_mov_b32_e32 v162, 0
	v_mov_b32_e32 v163, 0
	v_mov_b32_e32 v164, 0
	v_mov_b32_e32 v165, 0
	s_lshl_b32 s14, s52, 6
	s_and_b32 s14, s14, 0x7c0
	v_or_b32_e32 v84, s14, v1
	v_lshlrev_b32_e32 v2, 2, v84
	global_load_dword v134, v2, s[4:5]
	global_load_dword v135, v2, s[6:7]
	global_load_dword v136, v2, s[8:9]
	global_load_dword v137, v2, s[10:11]
	global_load_dword v138, v2, s[16:17]
	s_ashr_i32 s34, s52, 5
	s_ashr_i32 s35, s34, 31
	s_lshl_b64 s[34:35], s[34:35], 12
	s_add_u32 s36, s34, s56
	s_addc_u32 s37, s35, 0
	v_lshlrev_b32_e32 v82, 1, v84
	v_mov_b32_e32 v102, v83
	v_mov_b32_e32 v103, v83
	v_lshl_add_u64 v[86:87], s[24:25], 0, v[82:83]
	v_lshl_add_u64 v[88:89], s[26:27], 0, v[82:83]
	v_or_b32_e32 v82, 0x2000, v84
	v_or_b32_e32 v90, 0x4000, v84
	v_mov_b32_e32 v91, v83
	v_or_b32_e32 v92, 0x6000, v84
	v_mov_b32_e32 v93, v83
	v_or_b32_e32 v94, 0x8000, v84
	v_mov_b32_e32 v95, v83
	v_or_b32_e32 v96, 0xa000, v84
	v_mov_b32_e32 v97, v83
	v_or_b32_e32 v98, 0xc000, v84
	v_mov_b32_e32 v99, v83
	v_or_b32_e32 v100, 0xe000, v84
	v_mov_b32_e32 v101, v83
	s_lshl_b64 s[38:39], s[36:37], 11
	s_mov_b64 s[40:41], -1
	v_mov_b64_e32 v[104:105], v[102:103]
	v_mov_b64_e32 v[106:107], v[102:103]
	v_mov_b64_e32 v[108:109], v[102:103]
	v_mov_b64_e32 v[110:111], v[102:103]
	v_mov_b64_e32 v[112:113], v[102:103]
	v_mov_b64_e32 v[114:115], v[102:103]
	v_mov_b64_e32 v[116:117], v[102:103]
	s_mov_b32 s90, -1
	s_and_b64 vcc, exec, s[28:29]
	s_cbranch_vccz .Lpp_unit_skip
	s_and_b32 s78, s52, 31
	s_lshr_b32 s79, s52, 5
	s_lshl_b32 s80, s78, 8
	v_add_u32_e32 v48, s80, v236
	global_load_dwordx4 v[170:173], v48, s[4:5]
	global_load_dwordx4 v[174:177], v48, s[4:5] offset:16
	global_load_dwordx4 v[178:181], v48, s[6:7]
	global_load_dwordx4 v[182:185], v48, s[6:7] offset:16
	global_load_dwordx4 v[194:197], v48, s[8:9]
	global_load_dwordx4 v[198:201], v48, s[8:9] offset:16
	global_load_dwordx4 v[202:205], v48, s[10:11]
	global_load_dwordx4 v[206:209], v48, s[10:11] offset:16
	global_load_dwordx4 v[210:213], v48, s[16:17]
	global_load_dwordx4 v[214:217], v48, s[16:17] offset:16
	s_lshl_b32 s81, s79, 24
	s_lshl_b32 s78, s78, 7
	s_add_u32 s81, s81, s78
	s_add_u32 s56, s20, s81
	s_addc_u32 s57, s21, 0
	s_add_u32 s58, s20, s81
	s_addc_u32 s59, s21, 0
	s_add_u32 s58, s58, 0x8000000
	s_addc_u32 s59, s59, 0
	s_add_u32 s60, s20, s81
	s_addc_u32 s61, s21, 0
	s_add_u32 s60, s60, 0x10000000
	s_addc_u32 s61, s61, 0
	s_add_u32 s62, s22, s81
	s_addc_u32 s63, s23, 0
	s_add_u32 s66, s24, s81
	s_addc_u32 s67, s25, 0
	s_add_u32 s68, s26, s81
	s_addc_u32 s69, s27, 0
	s_lshl_b32 s81, s81, 1
	s_add_u32 s64, s18, s81
	s_addc_u32 s65, s19, 0
	global_load_dwordx4 v[2:5], v220, s[56:57]
	global_load_dwordx4 v[6:9], v220, s[58:59]
	global_load_dwordx4 v[10:13], v220, s[60:61]
	global_load_dwordx4 v[14:17], v220, s[62:63]
	global_load_dwordx4 v[18:21], v221, s[64:65]
	global_load_dwordx4 v[22:25], v221, s[64:65] offset:16
	s_add_u32 s56, s56, 0x20000
	s_addc_u32 s57, s57, 0
	s_add_u32 s58, s58, 0x20000
	s_addc_u32 s59, s59, 0
	s_add_u32 s60, s60, 0x20000
	s_addc_u32 s61, s61, 0
	s_add_u32 s62, s62, 0x20000
	s_addc_u32 s63, s63, 0
	s_add_u32 s64, s64, 0x40000
	s_addc_u32 s65, s65, 0
	s_waitcnt vmcnt(6)
	v_pk_add_f32 v[186:187], v[120:121], v[178:179] neg_lo:[0,1] neg_hi:[0,1]
	v_pk_add_f32 v[188:189], v[120:121], v[180:181] neg_lo:[0,1] neg_hi:[0,1]
	v_pk_add_f32 v[190:191], v[120:121], v[182:183] neg_lo:[0,1] neg_hi:[0,1]
	v_pk_add_f32 v[192:193], v[120:121], v[184:185] neg_lo:[0,1] neg_hi:[0,1]
.Lpp_unit_skip:
	s_branch .LBB0_3488

; __device__ __forceinline__ float fast_sigmoid(float x) { return __builtin_amdgcn_rcpf(1.0f + __expf(-x)); }
; #define LAS __attribute__((address_space(3)))
; __device__ __forceinline__ unsigned short f2bf(float f) { return (unsigned short)(pk2(f, 0.f) & 0xffffu); }
; template <class AT_>
; __device__ __forceinline__ void rwkv_scan_phase(const AT_& a, Frame& F, int j) {
;     ...
;                 if (do_post) {
; #pragma unroll
;                     for (int i = 0; i < 8; ++i) pg[i] = bf2f(GG[(tokb + (size_t)(blk - 1) * RW_T + tw + 4 * i) * DM + col]); }
;                 if (do_post) {
;                     const int pb = blk - 1; const LAS float* ob = (const LAS float*)(F.lds + (pb & 1) * OPB); const LAS float* Yb = Ybase + (pb & 1) * (RW_T * 64);
; #pragma unroll
;                     for (int i = 0; i < 8; ++i) { const int t = tw + 4 * i; const size_t tok = tokb + (size_t)pb * RW_T + t;
;                         const float y = Yb[t * 64 + lane], vv = ob[5 * RW_T * 64 + t * 64 + lane], bon = ob[6 * RW_T * 64 + t * 4 + 2];
;                         const float mu = wave_sum_dpp(y) * (1.0f / 64.0f), dlt = y - mu, var = wave_sum_dpp(dlt * dlt) * (1.0f / 64.0f);
;                         const float yn = dlt * __builtin_amdgcn_rsqf(var + RW_LN_EPS) * lnw + lnb + bon * vv;
;                         YG[tok * DM + col] = f2bf(yn * pg[i]); }
;                 }
;                 if (do_prep) {
;                     LAS float* ob = (LAS float*)(F.lds + ((blk + 1) & 1) * OPB);
; #pragma unroll
;                     for (int i = 0; i < 8; ++i) { const int t = tw + 4 * i; const float rr = pr[i], kk0 = pk[i], vv = pv[i];
;                         const float dec = __expf(-0.6065306597f * pg8::fast_sigmoid(pd[i])), ag = pg8::fast_sigmoid(pa[i]);
.LBB0_3488:
	s_mov_b64 s[42:43], -1
	s_and_b64 vcc, exec, s[28:29]
	s_cbranch_vccz .LBB0_3512
	s_waitcnt vmcnt(0)
	s_cmp_lt_i32 s90, 1
	s_cbranch_scc1 .Lpp_nopost
	s_add_i32 s78, s90, 1
	s_and_b32 s78, s78, 1
	s_mul_i32 s79, s78, 0xc200
	s_add_i32 s79, s79, s53
	s_lshl_b32 s78, s78, 13
	s_add_i32 s78, s78, s53
	s_add_i32 s78, s78, 0x18400
	v_add_u32_e32 v224, s78, v218
	v_add_u32_e32 v225, s79, v218
	v_add_u32_e32 v226, s79, v219
	ds_read_b128 v[30:33], v224
	ds_read_b128 v[34:37], v224 offset:16
	ds_read_b128 v[38:41], v225 offset:40960
	ds_read_b128 v[42:45], v225 offset:40976
	ds_read_b32 v46, v226 offset:49160
	v_lshlrev_b32_e32 v66, 16, v26
	v_and_b32_e32 v67, 0xffff0000, v26
	v_lshlrev_b32_e32 v68, 16, v27
	v_and_b32_e32 v69, 0xffff0000, v27
	v_lshlrev_b32_e32 v70, 16, v28
	v_and_b32_e32 v71, 0xffff0000, v28
	v_lshlrev_b32_e32 v72, 16, v29
	v_and_b32_e32 v73, 0xffff0000, v29
	s_waitcnt lgkmcnt(0)
	v_pk_add_f32 v[48:49], v[30:31], v[32:33]
	v_pk_add_f32 v[50:51], v[34:35], v[36:37]
	v_pk_add_f32 v[48:49], v[48:49], v[50:51]
	v_add_f32_e32 v52, v48, v49
	s_nop 1
	v_add_f32_dpp v52, v52, v52 quad_perm:[1,0,3,2] row_mask:0xf bank_mask:0xf bound_ctrl:1
	s_nop 1
	v_add_f32_dpp v52, v52, v52 quad_perm:[2,3,0,1] row_mask:0xf bank_mask:0xf bound_ctrl:1
	s_nop 1
	v_add_f32_dpp v52, v52, v52 row_half_mirror row_mask:0xf bank_mask:0xf bound_ctrl:1
	s_nop 1
	v_mul_f32_e32 v52, 0xbc800000, v52
	v_pk_add_f32 v[54:55], v[30:31], v[52:53] op_sel_hi:[1,0]
	v_pk_add_f32 v[56:57], v[32:33], v[52:53] op_sel_hi:[1,0]
	v_pk_add_f32 v[58:59], v[34:35], v[52:53] op_sel_hi:[1,0]
	v_pk_add_f32 v[60:61], v[36:37], v[52:53] op_sel_hi:[1,0]
	v_pk_mul_f32 v[62:63], v[54:55], v[54:55]
	v_pk_fma_f32 v[62:63], v[56:57], v[56:57], v[62:63]
	v_pk_fma_f32 v[62:63], v[58:59], v[58:59], v[62:63]
	v_pk_fma_f32 v[62:63], v[60:61], v[60:61], v[62:63]
	v_add_f32_e32 v64, v62, v63
	s_nop 1
	v_add_f32_dpp v64, v64, v64 quad_perm:[1,0,3,2] row_mask:0xf bank_mask:0xf bound_ctrl:1
	s_nop 1
	v_add_f32_dpp v64, v64, v64 quad_perm:[2,3,0,1] row_mask:0xf bank_mask:0xf bound_ctrl:1
	s_nop 1
	v_add_f32_dpp v64, v64, v64 row_half_mirror row_mask:0xf bank_mask:0xf bound_ctrl:1
	s_nop 1
	v_fma_f32 v64, v64, v222, v223
	v_rsq_f32_e32 v64, v64
	s_nop 0
	v_pk_mul_f32 v[54:55], v[54:55], v[64:65] op_sel_hi:[1,0]
	v_pk_mul_f32 v[56:57], v[56:57], v[64:65] op_sel_hi:[1,0]
	v_pk_mul_f32 v[58:59], v[58:59], v[64:65] op_sel_hi:[1,0]
	v_pk_mul_f32 v[60:61], v[60:61], v[64:65] op_sel_hi:[1,0]
	v_pk_fma_f32 v[54:55], v[54:55], v[202:203], v[210:211]
	v_pk_fma_f32 v[56:57], v[56:57], v[204:205], v[212:213]
	v_pk_fma_f32 v[58:59], v[58:59], v[206:207], v[214:215]
	v_pk_fma_f32 v[60:61], v[60:61], v[208:209], v[216:217]
	v_pk_fma_f32 v[54:55], v[38:39], v[46:47], v[54:55] op_sel_hi:[1,0,1]
	v_pk_fma_f32 v[56:57], v[40:41], v[46:47], v[56:57] op_sel_hi:[1,0,1]
	v_pk_fma_f32 v[58:59], v[42:43], v[46:47], v[58:59] op_sel_hi:[1,0,1]
	v_pk_fma_f32 v[60:61], v[44:45], v[46:47], v[60:61] op_sel_hi:[1,0,1]
	v_pk_mul_f32 v[54:55], v[54:55], v[66:67]
	v_pk_mul_f32 v[56:57], v[56:57], v[68:69]
	v_pk_mul_f32 v[58:59], v[58:59], v[70:71]
	v_pk_mul_f32 v[60:61], v[60:61], v[72:73]
	v_cvt_pk_bf16_f32 v74, v54, v55
	v_cvt_pk_bf16_f32 v75, v56, v57
	v_cvt_pk_bf16_f32 v76, v58, v59
	v_cvt_pk_bf16_f32 v77, v60, v61
	global_store_dwordx4 v220, v[74:77], s[68:69]
	s_add_u32 s68, s68, 0x20000
	s_addc_u32 s69, s69, 0
.Lpp_nopost:
	s_cmpk_gt_i32 s90, 0x7e
	s_cbranch_scc1 .Lpp_noprep
	v_lshlrev_b32_e32 v80, 16, v2
	v_and_b32_e32 v81, 0xffff0000, v2
	v_lshlrev_b32_e32 v82, 16, v3
	v_and_b32_e32 v83, 0xffff0000, v3
	v_lshlrev_b32_e32 v84, 16, v4
	v_and_b32_e32 v85, 0xffff0000, v4
	v_lshlrev_b32_e32 v86, 16, v5
	v_and_b32_e32 v87, 0xffff0000, v5
	v_lshlrev_b32_e32 v88, 16, v6
	v_and_b32_e32 v89, 0xffff0000, v6
	v_lshlrev_b32_e32 v90, 16, v7
	v_and_b32_e32 v91, 0xffff0000, v7
	v_lshlrev_b32_e32 v92, 16, v8
	v_and_b32_e32 v93, 0xffff0000, v8
	v_lshlrev_b32_e32 v94, 16, v9
	v_and_b32_e32 v95, 0xffff0000, v9
	v_lshlrev_b32_e32 v96, 16, v10
	v_and_b32_e32 v97, 0xffff0000, v10
	v_lshlrev_b32_e32 v98, 16, v11
	v_and_b32_e32 v99, 0xffff0000, v11
	v_lshlrev_b32_e32 v100, 16, v12
	v_and_b32_e32 v101, 0xffff0000, v12
	v_lshlrev_b32_e32 v102, 16, v13
	v_and_b32_e32 v103, 0xffff0000, v13
	v_lshlrev_b32_e32 v104, 16, v14
	v_and_b32_e32 v105, 0xffff0000, v14
	v_lshlrev_b32_e32 v106, 16, v15
	v_and_b32_e32 v107, 0xffff0000, v15
	v_lshlrev_b32_e32 v108, 16, v16
	v_and_b32_e32 v109, 0xffff0000, v16
	v_lshlrev_b32_e32 v110, 16, v17
	v_and_b32_e32 v111, 0xffff0000, v17
	v_pk_mul_f32 v[112:113], v[18:19], s[72:73] op_sel_hi:[1,0]
	v_pk_mul_f32 v[114:115], v[20:21], s[72:73] op_sel_hi:[1,0]
	v_pk_mul_f32 v[116:117], v[22:23], s[72:73] op_sel_hi:[1,0]
	v_pk_mul_f32 v[118:119], v[24:25], s[72:73] op_sel_hi:[1,0]
	v_exp_f32_e32 v112, v112
	v_exp_f32_e32 v113, v113
	v_exp_f32_e32 v114, v114
	v_exp_f32_e32 v115, v115
	v_exp_f32_e32 v116, v116
	v_exp_f32_e32 v117, v117
	v_exp_f32_e32 v118, v118
	v_exp_f32_e32 v119, v119
	v_pk_add_f32 v[112:113], v[112:113], v[120:121]
	v_pk_add_f32 v[114:115], v[114:115], v[120:121]
	v_pk_add_f32 v[116:117], v[116:117], v[120:121]
	v_pk_add_f32 v[118:119], v[118:119], v[120:121]
	v_rcp_f32_e32 v112, v112
	v_rcp_f32_e32 v113, v113
	v_rcp_f32_e32 v114, v114
	v_rcp_f32_e32 v115, v115
	v_rcp_f32_e32 v116, v116
	v_rcp_f32_e32 v117, v117
	v_rcp_f32_e32 v118, v118
	v_rcp_f32_e32 v119, v119
	v_pk_mul_f32 v[112:113], v[112:113], s[76:77] op_sel_hi:[1,0]
	v_pk_mul_f32 v[114:115], v[114:115], s[76:77] op_sel_hi:[1,0]
	v_pk_mul_f32 v[116:117], v[116:117], s[76:77] op_sel_hi:[1,0]
	v_pk_mul_f32 v[118:119], v[118:119], s[76:77] op_sel_hi:[1,0]
; __device__ __forceinline__ float fast_sigmoid(float x) { return __builtin_amdgcn_rcpf(1.0f + __expf(-x)); }
; template <class AT_>
; __device__ __forceinline__ void rwkv_scan_phase(const AT_& a, Frame& F, int j) {
;     ...
;                     for (int i = 0; i < 8; ++i) { const int t = tw + 4 * i; const float rr = pr[i], kk0 = pk[i], vv = pv[i];
;                         const float dec = __expf(-0.6065306597f * pg8::fast_sigmoid(pd[i])), ag = pg8::fast_sigmoid(pa[i]);
;                         float kkv = kk0 * kkc; kkv = kkv * __builtin_amdgcn_rsqf(fmaxf(wave_sum_dpp(kkv * kkv), 1e-24f));
;                         const float kp = kk0 * (1.0f + (ag - 1.0f) * kac); const float bv = kkv * ag;
;                         ob[t * 64 + lane] = -kkv; ob[RW_T * 64 + t * 64 + lane] = dec * rr; ob[2 * RW_T * 64 + t * 64 + lane] = dec;
;                         ob[3 * RW_T * 64 + t * 64 + lane] = bv; ob[4 * RW_T * 64 + t * 64 + lane] = kp; ob[5 * RW_T * 64 + t * 64 + lane] = vv;
;                         const float br = wave_sum_dpp(bv * rr), kr = wave_sum_dpp(kp * rr), bon = wave_sum_dpp(rr * kp * rkc);
;                         if (lane == 0) { ob[6 * RW_T * 64 + t * 4] = br; ob[6 * RW_T * 64 + t * 4 + 1] = kr; ob[6 * RW_T * 64 + t * 4 + 2] = bon; } }
	v_pk_mul_f32 v[112:113], v[112:113], s[74:75] op_sel_hi:[1,0]
	v_pk_mul_f32 v[114:115], v[114:115], s[74:75] op_sel_hi:[1,0]
	v_pk_mul_f32 v[116:117], v[116:117], s[74:75] op_sel_hi:[1,0]
	v_pk_mul_f32 v[118:119], v[118:119], s[74:75] op_sel_hi:[1,0]
	v_exp_f32_e32 v112, v112
	v_exp_f32_e32 v113, v113
	v_exp_f32_e32 v114, v114
	v_exp_f32_e32 v115, v115
	v_exp_f32_e32 v116, v116
	v_exp_f32_e32 v117, v117
	v_exp_f32_e32 v118, v118
	v_exp_f32_e32 v119, v119
	v_pk_mul_f32 v[122:123], v[104:105], s[72:73] op_sel_hi:[1,0]
	v_pk_mul_f32 v[124:125], v[106:107], s[72:73] op_sel_hi:[1,0]
	v_pk_mul_f32 v[126:127], v[108:109], s[72:73] op_sel_hi:[1,0]
	v_pk_mul_f32 v[128:129], v[110:111], s[72:73] op_sel_hi:[1,0]
	v_exp_f32_e32 v122, v122
	v_exp_f32_e32 v123, v123
	v_exp_f32_e32 v124, v124
	v_exp_f32_e32 v125, v125
	v_exp_f32_e32 v126, v126
	v_exp_f32_e32 v127, v127
	v_exp_f32_e32 v128, v128
	v_exp_f32_e32 v129, v129
	v_pk_add_f32 v[122:123], v[122:123], v[120:121]
	v_pk_add_f32 v[124:125], v[124:125], v[120:121]
	v_pk_add_f32 v[126:127], v[126:127], v[120:121]
	v_pk_add_f32 v[128:129], v[128:129], v[120:121]
	v_rcp_f32_e32 v122, v122
	v_rcp_f32_e32 v123, v123
	v_rcp_f32_e32 v124, v124
	v_rcp_f32_e32 v125, v125
	v_rcp_f32_e32 v126, v126
	v_rcp_f32_e32 v127, v127
	v_rcp_f32_e32 v128, v128
	v_rcp_f32_e32 v129, v129
	v_pk_mul_f32 v[130:131], v[88:89], v[170:171]
	v_pk_mul_f32 v[132:133], v[90:91], v[172:173]
	v_pk_mul_f32 v[134:135], v[92:93], v[174:175]
	v_pk_mul_f32 v[136:137], v[94:95], v[176:177]
	v_pk_mul_f32 v[138:139], v[130:131], v[130:131]
	v_pk_fma_f32 v[138:139], v[132:133], v[132:133], v[138:139]
	v_pk_fma_f32 v[138:139], v[134:135], v[134:135], v[138:139]
	v_pk_fma_f32 v[138:139], v[136:137], v[136:137], v[138:139]
	v_add_f32_e32 v140, v138, v139
	s_nop 1
	v_add_f32_dpp v140, v140, v140 quad_perm:[1,0,3,2] row_mask:0xf bank_mask:0xf bound_ctrl:1
	s_nop 1
	v_add_f32_dpp v140, v140, v140 quad_perm:[2,3,0,1] row_mask:0xf bank_mask:0xf bound_ctrl:1
	s_nop 1
	v_add_f32_dpp v140, v140, v140 row_half_mirror row_mask:0xf bank_mask:0xf bound_ctrl:1
	s_nop 1
	v_max_f32_e32 v140, 0x179abe15, v140
	v_rsq_f32_e32 v140, v140
	s_nop 0
	v_xor_b32_e32 v140, 0x80000000, v140
	v_pk_mul_f32 v[130:131], v[130:131], v[140:141] op_sel_hi:[1,0]
	v_pk_mul_f32 v[132:133], v[132:133], v[140:141] op_sel_hi:[1,0]
	v_pk_mul_f32 v[134:135], v[134:135], v[140:141] op_sel_hi:[1,0]
	v_pk_mul_f32 v[136:137], v[136:137], v[140:141] op_sel_hi:[1,0]
	v_pk_mul_f32 v[142:143], v[130:131], v[122:123] neg_lo:[1,0] neg_hi:[1,0]
	v_pk_mul_f32 v[144:145], v[132:133], v[124:125] neg_lo:[1,0] neg_hi:[1,0]
	v_pk_mul_f32 v[146:147], v[134:135], v[126:127] neg_lo:[1,0] neg_hi:[1,0]
	v_pk_mul_f32 v[148:149], v[136:137], v[128:129] neg_lo:[1,0] neg_hi:[1,0]
	v_pk_fma_f32 v[150:151], v[122:123], v[178:179], v[186:187]
	v_pk_fma_f32 v[152:153], v[124:125], v[180:181], v[188:189]
	v_pk_fma_f32 v[154:155], v[126:127], v[182:183], v[190:191]
	v_pk_fma_f32 v[156:157], v[128:129], v[184:185], v[192:193]
	v_pk_mul_f32 v[150:151], v[150:151], v[88:89]
	v_pk_mul_f32 v[152:153], v[152:153], v[90:91]
	v_pk_mul_f32 v[154:155], v[154:155], v[92:93]
	v_pk_mul_f32 v[156:157], v[156:157], v[94:95]
	v_pk_mul_f32 v[158:159], v[112:113], v[80:81]
	v_pk_mul_f32 v[160:161], v[114:115], v[82:83]
	v_pk_mul_f32 v[162:163], v[116:117], v[84:85]
	v_pk_mul_f32 v[164:165], v[118:119], v[86:87]
	v_pk_mul_f32 v[48:49], v[142:143], v[80:81]
	v_pk_fma_f32 v[48:49], v[144:145], v[82:83], v[48:49]
	v_pk_fma_f32 v[48:49], v[146:147], v[84:85], v[48:49]
	v_pk_fma_f32 v[48:49], v[148:149], v[86:87], v[48:49]
	v_pk_mul_f32 v[228:229], v[150:151], v[80:81]
	v_pk_mul_f32 v[230:231], v[152:153], v[82:83]
	v_pk_mul_f32 v[232:233], v[154:155], v[84:85]
	v_pk_mul_f32 v[234:235], v[156:157], v[86:87]
	v_pk_add_f32 v[50:51], v[228:229], v[230:231]
	v_pk_add_f32 v[52:53], v[232:233], v[234:235]
	v_pk_add_f32 v[50:51], v[50:51], v[52:53]
	v_pk_mul_f32 v[62:63], v[228:229], v[194:195]
	v_pk_fma_f32 v[62:63], v[230:231], v[196:197], v[62:63]
	v_pk_fma_f32 v[62:63], v[232:233], v[198:199], v[62:63]
	v_pk_fma_f32 v[62:63], v[234:235], v[200:201], v[62:63]
	v_add_f32_e32 v166, v48, v49
	v_add_f32_e32 v167, v50, v51
	v_add_f32_e32 v168, v62, v63
	v_add_f32_dpp v166, v166, v166 quad_perm:[1,0,3,2] row_mask:0xf bank_mask:0xf bound_ctrl:1
	v_add_f32_dpp v167, v167, v167 quad_perm:[1,0,3,2] row_mask:0xf bank_mask:0xf bound_ctrl:1
	v_add_f32_dpp v168, v168, v168 quad_perm:[1,0,3,2] row_mask:0xf bank_mask:0xf bound_ctrl:1
	v_add_f32_dpp v166, v166, v166 quad_perm:[2,3,0,1] row_mask:0xf bank_mask:0xf bound_ctrl:1
	v_add_f32_dpp v167, v167, v167 quad_perm:[2,3,0,1] row_mask:0xf bank_mask:0xf bound_ctrl:1
	v_add_f32_dpp v168, v168, v168 quad_perm:[2,3,0,1] row_mask:0xf bank_mask:0xf bound_ctrl:1
	v_add_f32_dpp v166, v166, v166 row_half_mirror row_mask:0xf bank_mask:0xf bound_ctrl:1
	v_add_f32_dpp v167, v167, v167 row_half_mirror row_mask:0xf bank_mask:0xf bound_ctrl:1
	v_add_f32_dpp v168, v168, v168 row_half_mirror row_mask:0xf bank_mask:0xf bound_ctrl:1
	s_add_i32 s78, s90, 1
	s_and_b32 s78, s78, 1
	s_mul_i32 s78, s78, 0xc200
	s_add_i32 s78, s78, s53
	v_add_u32_e32 v225, s78, v218
	v_add_u32_e32 v226, s78, v219
	ds_write_b128 v225, v[130:133] offset:0
	ds_write_b128 v225, v[134:137] offset:16
	ds_write_b128 v225, v[158:161] offset:8192
	ds_write_b128 v225, v[162:165] offset:8208
	ds_write_b128 v225, v[112:115] offset:16384
	ds_write_b128 v225, v[116:119] offset:16400
	ds_write_b128 v225, v[142:145] offset:24576
	ds_write_b128 v225, v[146:149] offset:24592
	ds_write_b128 v225, v[150:153] offset:32768
	ds_write_b128 v225, v[154:157] offset:32784
	ds_write_b128 v225, v[96:99] offset:40960
	ds_write_b128 v225, v[100:103] offset:40976
	s_mov_b64 exec, s[70:71]
	ds_write_b96 v226, v[166:168] offset:49152
	s_mov_b64 exec, -1
; #define LAS __attribute__((address_space(3)))
; template <class AT_>
; __device__ __forceinline__ void rwkv_scan_phase(const AT_& a, Frame& F, int j) {
;     ...
;             if (w < 4) {
;                 if (blk >= 0 && blk < RW_NBLK) {
;                     const LAS float* ob = (const LAS float*)(F.lds + (blk & 1) * OPB); LAS float* Yb = Ybase + (blk & 1) * (RW_T * 64);
;                     auto ld = [&](int t) { RwOps o; const LAS float* p = ob + t * 64 + 8 * kg;
;                         o.a0 = *(const LAS f32x4*)p; o.a1 = *(const LAS f32x4*)(p + 4); p += RW_T * 64; o.r0 = *(const LAS f32x4*)p; o.r1 = *(const LAS f32x4*)(p + 4); p += RW_T * 64;
;                         o.w0 = *(const LAS f32x4*)p; o.w1 = *(const LAS f32x4*)(p + 4); p += RW_T * 64; o.b0 = *(const LAS f32x4*)p; o.b1 = *(const LAS f32x4*)(p + 4); p += RW_T * 64;
;                         o.k0 = *(const LAS f32x4*)p; o.k1 = *(const LAS f32x4*)(p + 4);
;                         o.v = *(const LAS f32x2*)(ob + 5 * RW_T * 64 + t * 64 + v0); o.sc = *(const LAS f32x2*)(ob + 6 * RW_T * 64 + t * 4); return o; };
;                     auto step = [&](const RwOps& cur, int t) {
;                         const f32x2 a01 = {cur.a0.x, cur.a0.y}, a23 = {cur.a0.z, cur.a0.w}, a45 = {cur.a1.x, cur.a1.y}, a67 = {cur.a1.z, cur.a1.w};
;                         const f32x2 r01 = {cur.r0.x, cur.r0.y}, r23 = {cur.r0.z, cur.r0.w}, r45 = {cur.r1.x, cur.r1.y}, r67 = {cur.r1.z, cur.r1.w};
;                         f32x2 sA0 = S0[0] * a01, sA1 = S1[0] * a01, sY0 = S0[0] * r01, sY1 = S1[0] * r01;
;                         sA0 = S0[1] * a23 + sA0; sA1 = S1[1] * a23 + sA1; sY0 = S0[1] * r23 + sY0; sY1 = S1[1] * r23 + sY1;
;                         sA0 = S0[2] * a45 + sA0; sA1 = S1[2] * a45 + sA1; sY0 = S0[2] * r45 + sY0; sY1 = S1[2] * r45 + sY1;
;     ...
;                 if (do_prep) {
; #pragma unroll
;                     for (int i = 0; i < 8; ++i) { const size_t off = (tokb + (size_t)(blk + 1) * RW_T + tw + 4 * i) * DM + col;
;                         pr[i] = bf2f(RKV[off]); pk[i] = bf2f(RKV[(size_t)MTOK * DM + off]); pv[i] = bf2f(RKV[(size_t)2 * MTOK * DM + off]); pd[i] = DEC[off]; pa[i] = bf2f(AG[off]); } }
;                 if (do_post) {
; #pragma unroll
;                     for (int i = 0; i < 8; ++i) pg[i] = bf2f(GG[(tokb + (size_t)(blk - 1) * RW_T + tw + 4 * i) * DM + col]); }
.Lpp_noprep:
	s_cmpk_gt_i32 s90, 0x7d
	s_cbranch_scc1 .Lpp_nold
	global_load_dwordx4 v[2:5], v220, s[56:57]
	global_load_dwordx4 v[6:9], v220, s[58:59]
	global_load_dwordx4 v[10:13], v220, s[60:61]
	global_load_dwordx4 v[14:17], v220, s[62:63]
	global_load_dwordx4 v[18:21], v221, s[64:65]
	global_load_dwordx4 v[22:25], v221, s[64:65] offset:16
	s_add_u32 s56, s56, 0x20000
	s_addc_u32 s57, s57, 0
	s_add_u32 s58, s58, 0x20000
	s_addc_u32 s59, s59, 0
	s_add_u32 s60, s60, 0x20000
	s_addc_u32 s61, s61, 0
	s_add_u32 s62, s62, 0x20000
	s_addc_u32 s63, s63, 0
	s_add_u32 s64, s64, 0x40000
	s_addc_u32 s65, s65, 0
.Lpp_nold:
	s_cmp_lt_i32 s90, 0
	s_cbranch_scc1 .Lpp_nog
	s_cmpk_gt_i32 s90, 0x7f
	s_cbranch_scc1 .Lpp_nog
	global_load_dwordx4 v[26:29], v220, s[66:67]
	s_add_u32 s66, s66, 0x20000
	s_addc_u32 s67, s67, 0
.Lpp_nog:
.LBB0_3511:
	s_mov_b64 s[42:43], 0
.LBB0_3512:
	s_and_b64 vcc, exec, s[42:43]
	s_cbranch_vccz .LBB0_3487
	s_cmp_lt_i32 s90, 0
	s_cselect_b64 s[42:43], -1, 0
	s_cmpk_eq_i32 s90, 0x80
	s_cselect_b64 s[44:45], -1, 0
	s_or_b64 s[42:43], s[42:43], s[44:45]
	s_and_b64 vcc, exec, s[42:43]
	s_cbranch_vccnz .LBB0_3487
	s_and_b32 s98, s90, 1
	s_mul_i32 s99, s98, 0xc200
	s_add_i32 s99, s99, s53
	v_add_u32_e32 v50, s99, v166
	v_add_u32_e32 v51, s99, v167
	v_mov_b32_e32 v52, s99
	s_lshl_b32 s98, s98, 13
	s_add_i32 s98, s98, s53
	s_add_i32 s98, s98, 0x18400
	v_add_u32_e32 v53, s98, v167
	ds_read_b128 v[168:171], v50 offset:0
	ds_read_b128 v[172:175], v50 offset:16
	ds_read_b128 v[176:179], v50 offset:8192
	ds_read_b128 v[180:183], v50 offset:8208
	ds_read_b128 v[184:187], v50 offset:16384
	ds_read_b128 v[188:191], v50 offset:16400
	ds_read_b128 v[192:195], v50 offset:24576
	ds_read_b128 v[196:199], v50 offset:24592
	ds_read_b128 v[200:203], v50 offset:32768
	ds_read_b128 v[204:207], v50 offset:32784
	ds_read_b64 v[208:209], v51 offset:40960
	ds_read_b64 v[210:211], v52 offset:49152
	s_mov_b32 s98, 4
.Lscan_a_loop:
	s_waitcnt lgkmcnt(0)
	ds_read_b128 v[2:5], v50 offset:256
	ds_read_b128 v[6:9], v50 offset:272
	ds_read_b128 v[10:13], v50 offset:8448
	ds_read_b128 v[14:17], v50 offset:8464
	ds_read_b128 v[18:21], v50 offset:16640
	ds_read_b128 v[22:25], v50 offset:16656
	ds_read_b128 v[26:29], v50 offset:24832
	ds_read_b128 v[30:33], v50 offset:24848
	ds_read_b128 v[34:37], v50 offset:33024
	ds_read_b128 v[38:41], v50 offset:33040
	ds_read_b64 v[42:43], v51 offset:41216
	ds_read_b64 v[44:45], v52 offset:49168
	v_pk_mul_f32 v[46:47], v[150:151], v[168:169] op_sel_hi:[1,0]
	v_pk_mul_f32 v[48:49], v[150:151], v[176:177] op_sel_hi:[1,0]
	v_pk_fma_f32 v[46:47], v[152:153], v[168:169], v[46:47] op_sel:[0,1,0]
	v_pk_fma_f32 v[48:49], v[152:153], v[176:177], v[48:49] op_sel:[0,1,0]
	v_pk_fma_f32 v[46:47], v[154:155], v[170:171], v[46:47] op_sel_hi:[1,0,1]
	v_pk_fma_f32 v[48:49], v[154:155], v[178:179], v[48:49] op_sel_hi:[1,0,1]
	v_pk_fma_f32 v[46:47], v[156:157], v[170:171], v[46:47] op_sel:[0,1,0]
	v_pk_fma_f32 v[48:49], v[156:157], v[178:179], v[48:49] op_sel:[0,1,0]
	v_pk_fma_f32 v[46:47], v[158:159], v[172:173], v[46:47] op_sel_hi:[1,0,1]
	v_pk_fma_f32 v[48:49], v[158:159], v[180:181], v[48:49] op_sel_hi:[1,0,1]
	v_pk_fma_f32 v[46:47], v[160:161], v[172:173], v[46:47] op_sel:[0,1,0]
	v_pk_fma_f32 v[48:49], v[160:161], v[180:181], v[48:49] op_sel:[0,1,0]
	v_pk_fma_f32 v[46:47], v[162:163], v[174:175], v[46:47] op_sel_hi:[1,0,1]
	v_pk_fma_f32 v[48:49], v[162:163], v[182:183], v[48:49] op_sel_hi:[1,0,1]
	v_pk_fma_f32 v[46:47], v[164:165], v[174:175], v[46:47] op_sel:[0,1,0]
	v_pk_fma_f32 v[48:49], v[164:165], v[182:183], v[48:49] op_sel:[0,1,0]
	s_nop 0
	v_add_f32_dpp v46, v46, v46 quad_perm:[1,0,3,2] row_mask:0xf bank_mask:0xf bound_ctrl:1
	v_add_f32_dpp v47, v47, v47 quad_perm:[1,0,3,2] row_mask:0xf bank_mask:0xf bound_ctrl:1
	v_add_f32_dpp v48, v48, v48 quad_perm:[1,0,3,2] row_mask:0xf bank_mask:0xf bound_ctrl:1
	v_add_f32_dpp v49, v49, v49 quad_perm:[1,0,3,2] row_mask:0xf bank_mask:0xf bound_ctrl:1
	v_add_f32_dpp v46, v46, v46 quad_perm:[2,3,0,1] row_mask:0xf bank_mask:0xf bound_ctrl:1
	v_add_f32_dpp v47, v47, v47 quad_perm:[2,3,0,1] row_mask:0xf bank_mask:0xf bound_ctrl:1
	v_add_f32_dpp v48, v48, v48 quad_perm:[2,3,0,1] row_mask:0xf bank_mask:0xf bound_ctrl:1
	v_add_f32_dpp v49, v49, v49 quad_perm:[2,3,0,1] row_mask:0xf bank_mask:0xf bound_ctrl:1
	v_add_f32_dpp v46, v46, v46 row_half_mirror row_mask:0xf bank_mask:0xf bound_ctrl:1
	v_add_f32_dpp v47, v47, v47 row_half_mirror row_mask:0xf bank_mask:0xf bound_ctrl:1
	v_add_f32_dpp v48, v48, v48 row_half_mirror row_mask:0xf bank_mask:0xf bound_ctrl:1
	v_add_f32_dpp v49, v49, v49 row_half_mirror row_mask:0xf bank_mask:0xf bound_ctrl:1
	v_pk_fma_f32 v[48:49], v[46:47], v[210:211], v[48:49] op_sel_hi:[1,0,1]
	v_pk_fma_f32 v[48:49], v[208:209], v[210:211], v[48:49] op_sel:[0,1,0]
	s_mov_b64 exec, s[100:101]
	ds_write_b64 v53, v[48:49] offset:0
	s_mov_b64 exec, -1
	v_pk_mul_f32 v[150:151], v[150:151], v[184:185] op_sel_hi:[1,0]
	v_pk_mul_f32 v[152:153], v[152:153], v[184:185] op_sel:[0,1]
	v_pk_mul_f32 v[154:155], v[154:155], v[186:187] op_sel_hi:[1,0]
	v_pk_mul_f32 v[156:157], v[156:157], v[186:187] op_sel:[0,1]
	v_pk_mul_f32 v[158:159], v[158:159], v[188:189] op_sel_hi:[1,0]
	v_pk_mul_f32 v[160:161], v[160:161], v[188:189] op_sel:[0,1]
	v_pk_mul_f32 v[162:163], v[162:163], v[190:191] op_sel_hi:[1,0]
	v_pk_mul_f32 v[164:165], v[164:165], v[190:191] op_sel:[0,1]
	v_pk_fma_f32 v[150:151], v[46:47], v[192:193], v[150:151] op_sel_hi:[1,0,1]
	v_pk_fma_f32 v[152:153], v[46:47], v[192:193], v[152:153] op_sel:[0,1,0]
	v_pk_fma_f32 v[154:155], v[46:47], v[194:195], v[154:155] op_sel_hi:[1,0,1]
	v_pk_fma_f32 v[156:157], v[46:47], v[194:195], v[156:157] op_sel:[0,1,0]
	v_pk_fma_f32 v[158:159], v[46:47], v[196:197], v[158:159] op_sel_hi:[1,0,1]
	v_pk_fma_f32 v[160:161], v[46:47], v[196:197], v[160:161] op_sel:[0,1,0]
	v_pk_fma_f32 v[162:163], v[46:47], v[198:199], v[162:163] op_sel_hi:[1,0,1]
	v_pk_fma_f32 v[164:165], v[46:47], v[198:199], v[164:165] op_sel:[0,1,0]
	v_pk_fma_f32 v[150:151], v[208:209], v[200:201], v[150:151] op_sel_hi:[1,0,1]
	v_pk_fma_f32 v[152:153], v[208:209], v[200:201], v[152:153] op_sel:[0,1,0]
	v_pk_fma_f32 v[154:155], v[208:209], v[202:203], v[154:155] op_sel_hi:[1,0,1]
	v_pk_fma_f32 v[156:157], v[208:209], v[202:203], v[156:157] op_sel:[0,1,0]
	v_pk_fma_f32 v[158:159], v[208:209], v[204:205], v[158:159] op_sel_hi:[1,0,1]
	v_pk_fma_f32 v[160:161], v[208:209], v[204:205], v[160:161] op_sel:[0,1,0]
	v_pk_fma_f32 v[162:163], v[208:209], v[206:207], v[162:163] op_sel_hi:[1,0,1]
	v_pk_fma_f32 v[164:165], v[208:209], v[206:207], v[164:165] op_sel:[0,1,0]
	s_waitcnt lgkmcnt(0)
; template <class AT_>
; __device__ __forceinline__ void rwkv_scan_phase(const AT_& a, Frame& F, int j) {
;     ...
;                     auto step = [&](const RwOps& cur, int t) {
;                         const f32x2 a01 = {cur.a0.x, cur.a0.y}, a23 = {cur.a0.z, cur.a0.w}, a45 = {cur.a1.x, cur.a1.y}, a67 = {cur.a1.z, cur.a1.w};
;                         const f32x2 r01 = {cur.r0.x, cur.r0.y}, r23 = {cur.r0.z, cur.r0.w}, r45 = {cur.r1.x, cur.r1.y}, r67 = {cur.r1.z, cur.r1.w};
;                         f32x2 sA0 = S0[0] * a01, sA1 = S1[0] * a01, sY0 = S0[0] * r01, sY1 = S1[0] * r01;
;                         sA0 = S0[1] * a23 + sA0; sA1 = S1[1] * a23 + sA1; sY0 = S0[1] * r23 + sY0; sY1 = S1[1] * r23 + sY1;
;                         sA0 = S0[2] * a45 + sA0; sA1 = S1[2] * a45 + sA1; sY0 = S0[2] * r45 + sY0; sY1 = S1[2] * r45 + sY1;
;                         sA0 = S0[3] * a67 + sA0; sA1 = S1[3] * a67 + sA1; sY0 = S0[3] * r67 + sY0; sY1 = S1[3] * r67 + sY1;
;                         const float sa0 = row8_allsum(sA0.x + sA0.y), sa1 = row8_allsum(sA1.x + sA1.y), yy0 = row8_allsum(sY0.x + sY0.y), yy1 = row8_allsum(sY1.x + sY1.y);
;                         if (kg == 0) { f32x2 yo; yo.x = yy0 + sa0 * cur.sc.x + cur.v.x * cur.sc.y; yo.y = yy1 + sa1 * cur.sc.x + cur.v.y * cur.sc.y; *(LAS f32x2*)(Yb + t * 64 + v0) = yo; }
;                         const f32x2 w01 = {cur.w0.x, cur.w0.y}, w23 = {cur.w0.z, cur.w0.w}, w45 = {cur.w1.x, cur.w1.y}, w67 = {cur.w1.z, cur.w1.w};
;                         const f32x2 b01 = {cur.b0.x, cur.b0.y}, b23 = {cur.b0.z, cur.b0.w}, b45 = {cur.b1.x, cur.b1.y}, b67 = {cur.b1.z, cur.b1.w};
;                         const f32x2 k01 = {cur.k0.x, cur.k0.y}, k23 = {cur.k0.z, cur.k0.w}, k45 = {cur.k1.x, cur.k1.y}, k67 = {cur.k1.z, cur.k1.w};
;                         const f32x2 s0 = {sa0, sa0}, s1 = {sa1, sa1}, x0 = {cur.v.x, cur.v.x}, x1 = {cur.v.y, cur.v.y};
;                         S0[0] = S0[0] * w01 + (s0 * b01 + x0 * k01); S0[1] = S0[1] * w23 + (s0 * b23 + x0 * k23); S0[2] = S0[2] * w45 + (s0 * b45 + x0 * k45); S0[3] = S0[3] * w67 + (s0 * b67 + x0 * k67);
;                         S1[0] = S1[0] * w01 + (s1 * b01 + x1 * k01); S1[1] = S1[1] * w23 + (s1 * b23 + x1 * k23); S1[2] = S1[2] * w45 + (s1 * b45 + x1 * k45); S1[3] = S1[3] * w67 + (s1 * b67 + x1 * k67);
;                     };
;                     RwOps oa = ld(0);
	ds_read_b128 v[168:171], v50 offset:512
	ds_read_b128 v[172:175], v50 offset:528
	ds_read_b128 v[176:179], v50 offset:8704
	ds_read_b128 v[180:183], v50 offset:8720
	ds_read_b128 v[184:187], v50 offset:16896
	ds_read_b128 v[188:191], v50 offset:16912
	ds_read_b128 v[192:195], v50 offset:25088
	ds_read_b128 v[196:199], v50 offset:25104
	ds_read_b128 v[200:203], v50 offset:33280
	ds_read_b128 v[204:207], v50 offset:33296
	ds_read_b64 v[208:209], v51 offset:41472
	ds_read_b64 v[210:211], v52 offset:49184
	v_pk_mul_f32 v[46:47], v[150:151], v[2:3] op_sel_hi:[1,0]
	v_pk_mul_f32 v[48:49], v[150:151], v[10:11] op_sel_hi:[1,0]
	v_pk_fma_f32 v[46:47], v[152:153], v[2:3], v[46:47] op_sel:[0,1,0]
	v_pk_fma_f32 v[48:49], v[152:153], v[10:11], v[48:49] op_sel:[0,1,0]
	v_pk_fma_f32 v[46:47], v[154:155], v[4:5], v[46:47] op_sel_hi:[1,0,1]
	v_pk_fma_f32 v[48:49], v[154:155], v[12:13], v[48:49] op_sel_hi:[1,0,1]
	v_pk_fma_f32 v[46:47], v[156:157], v[4:5], v[46:47] op_sel:[0,1,0]
	v_pk_fma_f32 v[48:49], v[156:157], v[12:13], v[48:49] op_sel:[0,1,0]
	v_pk_fma_f32 v[46:47], v[158:159], v[6:7], v[46:47] op_sel_hi:[1,0,1]
	v_pk_fma_f32 v[48:49], v[158:159], v[14:15], v[48:49] op_sel_hi:[1,0,1]
	v_pk_fma_f32 v[46:47], v[160:161], v[6:7], v[46:47] op_sel:[0,1,0]
	v_pk_fma_f32 v[48:49], v[160:161], v[14:15], v[48:49] op_sel:[0,1,0]
	v_pk_fma_f32 v[46:47], v[162:163], v[8:9], v[46:47] op_sel_hi:[1,0,1]
	v_pk_fma_f32 v[48:49], v[162:163], v[16:17], v[48:49] op_sel_hi:[1,0,1]
	v_pk_fma_f32 v[46:47], v[164:165], v[8:9], v[46:47] op_sel:[0,1,0]
	v_pk_fma_f32 v[48:49], v[164:165], v[16:17], v[48:49] op_sel:[0,1,0]
	s_nop 0
	v_add_f32_dpp v46, v46, v46 quad_perm:[1,0,3,2] row_mask:0xf bank_mask:0xf bound_ctrl:1
	v_add_f32_dpp v47, v47, v47 quad_perm:[1,0,3,2] row_mask:0xf bank_mask:0xf bound_ctrl:1
	v_add_f32_dpp v48, v48, v48 quad_perm:[1,0,3,2] row_mask:0xf bank_mask:0xf bound_ctrl:1
	v_add_f32_dpp v49, v49, v49 quad_perm:[1,0,3,2] row_mask:0xf bank_mask:0xf bound_ctrl:1
	v_add_f32_dpp v46, v46, v46 quad_perm:[2,3,0,1] row_mask:0xf bank_mask:0xf bound_ctrl:1
	v_add_f32_dpp v47, v47, v47 quad_perm:[2,3,0,1] row_mask:0xf bank_mask:0xf bound_ctrl:1
	v_add_f32_dpp v48, v48, v48 quad_perm:[2,3,0,1] row_mask:0xf bank_mask:0xf bound_ctrl:1
	v_add_f32_dpp v49, v49, v49 quad_perm:[2,3,0,1] row_mask:0xf bank_mask:0xf bound_ctrl:1
	v_add_f32_dpp v46, v46, v46 row_half_mirror row_mask:0xf bank_mask:0xf bound_ctrl:1
	v_add_f32_dpp v47, v47, v47 row_half_mirror row_mask:0xf bank_mask:0xf bound_ctrl:1
	v_add_f32_dpp v48, v48, v48 row_half_mirror row_mask:0xf bank_mask:0xf bound_ctrl:1
	v_add_f32_dpp v49, v49, v49 row_half_mirror row_mask:0xf bank_mask:0xf bound_ctrl:1
	v_pk_fma_f32 v[48:49], v[46:47], v[44:45], v[48:49] op_sel_hi:[1,0,1]
	v_pk_fma_f32 v[48:49], v[42:43], v[44:45], v[48:49] op_sel:[0,1,0]
	s_mov_b64 exec, s[100:101]
	ds_write_b64 v53, v[48:49] offset:256
	s_mov_b64 exec, -1
	v_pk_mul_f32 v[150:151], v[150:151], v[18:19] op_sel_hi:[1,0]
	v_pk_mul_f32 v[152:153], v[152:153], v[18:19] op_sel:[0,1]
	v_pk_mul_f32 v[154:155], v[154:155], v[20:21] op_sel_hi:[1,0]
	v_pk_mul_f32 v[156:157], v[156:157], v[20:21] op_sel:[0,1]
	v_pk_mul_f32 v[158:159], v[158:159], v[22:23] op_sel_hi:[1,0]
	v_pk_mul_f32 v[160:161], v[160:161], v[22:23] op_sel:[0,1]
	v_pk_mul_f32 v[162:163], v[162:163], v[24:25] op_sel_hi:[1,0]
	v_pk_mul_f32 v[164:165], v[164:165], v[24:25] op_sel:[0,1]
	v_pk_fma_f32 v[150:151], v[46:47], v[26:27], v[150:151] op_sel_hi:[1,0,1]
	v_pk_fma_f32 v[152:153], v[46:47], v[26:27], v[152:153] op_sel:[0,1,0]
	v_pk_fma_f32 v[154:155], v[46:47], v[28:29], v[154:155] op_sel_hi:[1,0,1]
	v_pk_fma_f32 v[156:157], v[46:47], v[28:29], v[156:157] op_sel:[0,1,0]
	v_pk_fma_f32 v[158:159], v[46:47], v[30:31], v[158:159] op_sel_hi:[1,0,1]
	v_pk_fma_f32 v[160:161], v[46:47], v[30:31], v[160:161] op_sel:[0,1,0]
	v_pk_fma_f32 v[162:163], v[46:47], v[32:33], v[162:163] op_sel_hi:[1,0,1]
	v_pk_fma_f32 v[164:165], v[46:47], v[32:33], v[164:165] op_sel:[0,1,0]
	v_pk_fma_f32 v[150:151], v[42:43], v[34:35], v[150:151] op_sel_hi:[1,0,1]
	v_pk_fma_f32 v[152:153], v[42:43], v[34:35], v[152:153] op_sel:[0,1,0]
	v_pk_fma_f32 v[154:155], v[42:43], v[36:37], v[154:155] op_sel_hi:[1,0,1]
	v_pk_fma_f32 v[156:157], v[42:43], v[36:37], v[156:157] op_sel:[0,1,0]
	v_pk_fma_f32 v[158:159], v[42:43], v[38:39], v[158:159] op_sel_hi:[1,0,1]
	v_pk_fma_f32 v[160:161], v[42:43], v[38:39], v[160:161] op_sel:[0,1,0]
	v_pk_fma_f32 v[162:163], v[42:43], v[40:41], v[162:163] op_sel_hi:[1,0,1]
	v_pk_fma_f32 v[164:165], v[42:43], v[40:41], v[164:165] op_sel:[0,1,0]
	s_waitcnt lgkmcnt(0)
; template <class AT_>
; __device__ __forceinline__ void rwkv_scan_phase(const AT_& a, Frame& F, int j) {
;     ...
;                     auto step = [&](const RwOps& cur, int t) {
;                         const f32x2 a01 = {cur.a0.x, cur.a0.y}, a23 = {cur.a0.z, cur.a0.w}, a45 = {cur.a1.x, cur.a1.y}, a67 = {cur.a1.z, cur.a1.w};
;                         const f32x2 r01 = {cur.r0.x, cur.r0.y}, r23 = {cur.r0.z, cur.r0.w}, r45 = {cur.r1.x, cur.r1.y}, r67 = {cur.r1.z, cur.r1.w};
;                         f32x2 sA0 = S0[0] * a01, sA1 = S1[0] * a01, sY0 = S0[0] * r01, sY1 = S1[0] * r01;
;                         sA0 = S0[1] * a23 + sA0; sA1 = S1[1] * a23 + sA1; sY0 = S0[1] * r23 + sY0; sY1 = S1[1] * r23 + sY1;
;                         sA0 = S0[2] * a45 + sA0; sA1 = S1[2] * a45 + sA1; sY0 = S0[2] * r45 + sY0; sY1 = S1[2] * r45 + sY1;
;                         sA0 = S0[3] * a67 + sA0; sA1 = S1[3] * a67 + sA1; sY0 = S0[3] * r67 + sY0; sY1 = S1[3] * r67 + sY1;
;                         const float sa0 = row8_allsum(sA0.x + sA0.y), sa1 = row8_allsum(sA1.x + sA1.y), yy0 = row8_allsum(sY0.x + sY0.y), yy1 = row8_allsum(sY1.x + sY1.y);
;                         if (kg == 0) { f32x2 yo; yo.x = yy0 + sa0 * cur.sc.x + cur.v.x * cur.sc.y; yo.y = yy1 + sa1 * cur.sc.x + cur.v.y * cur.sc.y; *(LAS f32x2*)(Yb + t * 64 + v0) = yo; }
;                         const f32x2 w01 = {cur.w0.x, cur.w0.y}, w23 = {cur.w0.z, cur.w0.w}, w45 = {cur.w1.x, cur.w1.y}, w67 = {cur.w1.z, cur.w1.w};
;                         const f32x2 b01 = {cur.b0.x, cur.b0.y}, b23 = {cur.b0.z, cur.b0.w}, b45 = {cur.b1.x, cur.b1.y}, b67 = {cur.b1.z, cur.b1.w};
;                         const f32x2 k01 = {cur.k0.x, cur.k0.y}, k23 = {cur.k0.z, cur.k0.w}, k45 = {cur.k1.x, cur.k1.y}, k67 = {cur.k1.z, cur.k1.w};
;                         const f32x2 s0 = {sa0, sa0}, s1 = {sa1, sa1}, x0 = {cur.v.x, cur.v.x}, x1 = {cur.v.y, cur.v.y};
;                         S0[0] = S0[0] * w01 + (s0 * b01 + x0 * k01); S0[1] = S0[1] * w23 + (s0 * b23 + x0 * k23); S0[2] = S0[2] * w45 + (s0 * b45 + x0 * k45); S0[3] = S0[3] * w67 + (s0 * b67 + x0 * k67);
;                         S1[0] = S1[0] * w01 + (s1 * b01 + x1 * k01); S1[1] = S1[1] * w23 + (s1 * b23 + x1 * k23); S1[2] = S1[2] * w45 + (s1 * b45 + x1 * k45); S1[3] = S1[3] * w67 + (s1 * b67 + x1 * k67);
;                     };
;                     RwOps oa = ld(0);
	ds_read_b128 v[2:5], v50 offset:768
	ds_read_b128 v[6:9], v50 offset:784
	ds_read_b128 v[10:13], v50 offset:8960
	ds_read_b128 v[14:17], v50 offset:8976
	ds_read_b128 v[18:21], v50 offset:17152
	ds_read_b128 v[22:25], v50 offset:17168
	ds_read_b128 v[26:29], v50 offset:25344
	ds_read_b128 v[30:33], v50 offset:25360
	ds_read_b128 v[34:37], v50 offset:33536
	ds_read_b128 v[38:41], v50 offset:33552
	ds_read_b64 v[42:43], v51 offset:41728
	ds_read_b64 v[44:45], v52 offset:49200
	v_pk_mul_f32 v[46:47], v[150:151], v[168:169] op_sel_hi:[1,0]
	v_pk_mul_f32 v[48:49], v[150:151], v[176:177] op_sel_hi:[1,0]
	v_pk_fma_f32 v[46:47], v[152:153], v[168:169], v[46:47] op_sel:[0,1,0]
	v_pk_fma_f32 v[48:49], v[152:153], v[176:177], v[48:49] op_sel:[0,1,0]
	v_pk_fma_f32 v[46:47], v[154:155], v[170:171], v[46:47] op_sel_hi:[1,0,1]
	v_pk_fma_f32 v[48:49], v[154:155], v[178:179], v[48:49] op_sel_hi:[1,0,1]
	v_pk_fma_f32 v[46:47], v[156:157], v[170:171], v[46:47] op_sel:[0,1,0]
	v_pk_fma_f32 v[48:49], v[156:157], v[178:179], v[48:49] op_sel:[0,1,0]
	v_pk_fma_f32 v[46:47], v[158:159], v[172:173], v[46:47] op_sel_hi:[1,0,1]
	v_pk_fma_f32 v[48:49], v[158:159], v[180:181], v[48:49] op_sel_hi:[1,0,1]
	v_pk_fma_f32 v[46:47], v[160:161], v[172:173], v[46:47] op_sel:[0,1,0]
	v_pk_fma_f32 v[48:49], v[160:161], v[180:181], v[48:49] op_sel:[0,1,0]
	v_pk_fma_f32 v[46:47], v[162:163], v[174:175], v[46:47] op_sel_hi:[1,0,1]
	v_pk_fma_f32 v[48:49], v[162:163], v[182:183], v[48:49] op_sel_hi:[1,0,1]
	v_pk_fma_f32 v[46:47], v[164:165], v[174:175], v[46:47] op_sel:[0,1,0]
	v_pk_fma_f32 v[48:49], v[164:165], v[182:183], v[48:49] op_sel:[0,1,0]
	s_nop 0
	v_add_f32_dpp v46, v46, v46 quad_perm:[1,0,3,2] row_mask:0xf bank_mask:0xf bound_ctrl:1
	v_add_f32_dpp v47, v47, v47 quad_perm:[1,0,3,2] row_mask:0xf bank_mask:0xf bound_ctrl:1
	v_add_f32_dpp v48, v48, v48 quad_perm:[1,0,3,2] row_mask:0xf bank_mask:0xf bound_ctrl:1
	v_add_f32_dpp v49, v49, v49 quad_perm:[1,0,3,2] row_mask:0xf bank_mask:0xf bound_ctrl:1
	v_add_f32_dpp v46, v46, v46 quad_perm:[2,3,0,1] row_mask:0xf bank_mask:0xf bound_ctrl:1
	v_add_f32_dpp v47, v47, v47 quad_perm:[2,3,0,1] row_mask:0xf bank_mask:0xf bound_ctrl:1
	v_add_f32_dpp v48, v48, v48 quad_perm:[2,3,0,1] row_mask:0xf bank_mask:0xf bound_ctrl:1
	v_add_f32_dpp v49, v49, v49 quad_perm:[2,3,0,1] row_mask:0xf bank_mask:0xf bound_ctrl:1
	v_add_f32_dpp v46, v46, v46 row_half_mirror row_mask:0xf bank_mask:0xf bound_ctrl:1
	v_add_f32_dpp v47, v47, v47 row_half_mirror row_mask:0xf bank_mask:0xf bound_ctrl:1
	v_add_f32_dpp v48, v48, v48 row_half_mirror row_mask:0xf bank_mask:0xf bound_ctrl:1
	v_add_f32_dpp v49, v49, v49 row_half_mirror row_mask:0xf bank_mask:0xf bound_ctrl:1
	v_pk_fma_f32 v[48:49], v[46:47], v[210:211], v[48:49] op_sel_hi:[1,0,1]
	v_pk_fma_f32 v[48:49], v[208:209], v[210:211], v[48:49] op_sel:[0,1,0]
	s_mov_b64 exec, s[100:101]
	ds_write_b64 v53, v[48:49] offset:512
	s_mov_b64 exec, -1
	v_pk_mul_f32 v[150:151], v[150:151], v[184:185] op_sel_hi:[1,0]
	v_pk_mul_f32 v[152:153], v[152:153], v[184:185] op_sel:[0,1]
	v_pk_mul_f32 v[154:155], v[154:155], v[186:187] op_sel_hi:[1,0]
	v_pk_mul_f32 v[156:157], v[156:157], v[186:187] op_sel:[0,1]
	v_pk_mul_f32 v[158:159], v[158:159], v[188:189] op_sel_hi:[1,0]
	v_pk_mul_f32 v[160:161], v[160:161], v[188:189] op_sel:[0,1]
	v_pk_mul_f32 v[162:163], v[162:163], v[190:191] op_sel_hi:[1,0]
	v_pk_mul_f32 v[164:165], v[164:165], v[190:191] op_sel:[0,1]
	v_pk_fma_f32 v[150:151], v[46:47], v[192:193], v[150:151] op_sel_hi:[1,0,1]
	v_pk_fma_f32 v[152:153], v[46:47], v[192:193], v[152:153] op_sel:[0,1,0]
	v_pk_fma_f32 v[154:155], v[46:47], v[194:195], v[154:155] op_sel_hi:[1,0,1]
	v_pk_fma_f32 v[156:157], v[46:47], v[194:195], v[156:157] op_sel:[0,1,0]
	v_pk_fma_f32 v[158:159], v[46:47], v[196:197], v[158:159] op_sel_hi:[1,0,1]
	v_pk_fma_f32 v[160:161], v[46:47], v[196:197], v[160:161] op_sel:[0,1,0]
	v_pk_fma_f32 v[162:163], v[46:47], v[198:199], v[162:163] op_sel_hi:[1,0,1]
	v_pk_fma_f32 v[164:165], v[46:47], v[198:199], v[164:165] op_sel:[0,1,0]
	v_pk_fma_f32 v[150:151], v[208:209], v[200:201], v[150:151] op_sel_hi:[1,0,1]
	v_pk_fma_f32 v[152:153], v[208:209], v[200:201], v[152:153] op_sel:[0,1,0]
	v_pk_fma_f32 v[154:155], v[208:209], v[202:203], v[154:155] op_sel_hi:[1,0,1]
	v_pk_fma_f32 v[156:157], v[208:209], v[202:203], v[156:157] op_sel:[0,1,0]
	v_pk_fma_f32 v[158:159], v[208:209], v[204:205], v[158:159] op_sel_hi:[1,0,1]
	v_pk_fma_f32 v[160:161], v[208:209], v[204:205], v[160:161] op_sel:[0,1,0]
	v_pk_fma_f32 v[162:163], v[208:209], v[206:207], v[162:163] op_sel_hi:[1,0,1]
	v_pk_fma_f32 v[164:165], v[208:209], v[206:207], v[164:165] op_sel:[0,1,0]
	s_waitcnt lgkmcnt(0)
; template <class AT_>
; __device__ __forceinline__ void rwkv_scan_phase(const AT_& a, Frame& F, int j) {
;     ...
;                     auto step = [&](const RwOps& cur, int t) {
;                         const f32x2 a01 = {cur.a0.x, cur.a0.y}, a23 = {cur.a0.z, cur.a0.w}, a45 = {cur.a1.x, cur.a1.y}, a67 = {cur.a1.z, cur.a1.w};
;                         const f32x2 r01 = {cur.r0.x, cur.r0.y}, r23 = {cur.r0.z, cur.r0.w}, r45 = {cur.r1.x, cur.r1.y}, r67 = {cur.r1.z, cur.r1.w};
;                         f32x2 sA0 = S0[0] * a01, sA1 = S1[0] * a01, sY0 = S0[0] * r01, sY1 = S1[0] * r01;
;                         sA0 = S0[1] * a23 + sA0; sA1 = S1[1] * a23 + sA1; sY0 = S0[1] * r23 + sY0; sY1 = S1[1] * r23 + sY1;
;                         sA0 = S0[2] * a45 + sA0; sA1 = S1[2] * a45 + sA1; sY0 = S0[2] * r45 + sY0; sY1 = S1[2] * r45 + sY1;
;                         sA0 = S0[3] * a67 + sA0; sA1 = S1[3] * a67 + sA1; sY0 = S0[3] * r67 + sY0; sY1 = S1[3] * r67 + sY1;
;                         const float sa0 = row8_allsum(sA0.x + sA0.y), sa1 = row8_allsum(sA1.x + sA1.y), yy0 = row8_allsum(sY0.x + sY0.y), yy1 = row8_allsum(sY1.x + sY1.y);
;                         if (kg == 0) { f32x2 yo; yo.x = yy0 + sa0 * cur.sc.x + cur.v.x * cur.sc.y; yo.y = yy1 + sa1 * cur.sc.x + cur.v.y * cur.sc.y; *(LAS f32x2*)(Yb + t * 64 + v0) = yo; }
;                         const f32x2 w01 = {cur.w0.x, cur.w0.y}, w23 = {cur.w0.z, cur.w0.w}, w45 = {cur.w1.x, cur.w1.y}, w67 = {cur.w1.z, cur.w1.w};
;                         const f32x2 b01 = {cur.b0.x, cur.b0.y}, b23 = {cur.b0.z, cur.b0.w}, b45 = {cur.b1.x, cur.b1.y}, b67 = {cur.b1.z, cur.b1.w};
;                         const f32x2 k01 = {cur.k0.x, cur.k0.y}, k23 = {cur.k0.z, cur.k0.w}, k45 = {cur.k1.x, cur.k1.y}, k67 = {cur.k1.z, cur.k1.w};
;                         const f32x2 s0 = {sa0, sa0}, s1 = {sa1, sa1}, x0 = {cur.v.x, cur.v.x}, x1 = {cur.v.y, cur.v.y};
;                         S0[0] = S0[0] * w01 + (s0 * b01 + x0 * k01); S0[1] = S0[1] * w23 + (s0 * b23 + x0 * k23); S0[2] = S0[2] * w45 + (s0 * b45 + x0 * k45); S0[3] = S0[3] * w67 + (s0 * b67 + x0 * k67);
;                         S1[0] = S1[0] * w01 + (s1 * b01 + x1 * k01); S1[1] = S1[1] * w23 + (s1 * b23 + x1 * k23); S1[2] = S1[2] * w45 + (s1 * b45 + x1 * k45); S1[3] = S1[3] * w67 + (s1 * b67 + x1 * k67);
;                     };
;                     RwOps oa = ld(0);
	ds_read_b128 v[168:171], v50 offset:1024
	ds_read_b128 v[172:175], v50 offset:1040
	ds_read_b128 v[176:179], v50 offset:9216
	ds_read_b128 v[180:183], v50 offset:9232
	ds_read_b128 v[184:187], v50 offset:17408
	ds_read_b128 v[188:191], v50 offset:17424
	ds_read_b128 v[192:195], v50 offset:25600
	ds_read_b128 v[196:199], v50 offset:25616
	ds_read_b128 v[200:203], v50 offset:33792
	ds_read_b128 v[204:207], v50 offset:33808
	ds_read_b64 v[208:209], v51 offset:41984
	ds_read_b64 v[210:211], v52 offset:49216
	v_pk_mul_f32 v[46:47], v[150:151], v[2:3] op_sel_hi:[1,0]
	v_pk_mul_f32 v[48:49], v[150:151], v[10:11] op_sel_hi:[1,0]
	v_pk_fma_f32 v[46:47], v[152:153], v[2:3], v[46:47] op_sel:[0,1,0]
	v_pk_fma_f32 v[48:49], v[152:153], v[10:11], v[48:49] op_sel:[0,1,0]
	v_pk_fma_f32 v[46:47], v[154:155], v[4:5], v[46:47] op_sel_hi:[1,0,1]
	v_pk_fma_f32 v[48:49], v[154:155], v[12:13], v[48:49] op_sel_hi:[1,0,1]
	v_pk_fma_f32 v[46:47], v[156:157], v[4:5], v[46:47] op_sel:[0,1,0]
	v_pk_fma_f32 v[48:49], v[156:157], v[12:13], v[48:49] op_sel:[0,1,0]
	v_pk_fma_f32 v[46:47], v[158:159], v[6:7], v[46:47] op_sel_hi:[1,0,1]
	v_pk_fma_f32 v[48:49], v[158:159], v[14:15], v[48:49] op_sel_hi:[1,0,1]
	v_pk_fma_f32 v[46:47], v[160:161], v[6:7], v[46:47] op_sel:[0,1,0]
	v_pk_fma_f32 v[48:49], v[160:161], v[14:15], v[48:49] op_sel:[0,1,0]
	v_pk_fma_f32 v[46:47], v[162:163], v[8:9], v[46:47] op_sel_hi:[1,0,1]
	v_pk_fma_f32 v[48:49], v[162:163], v[16:17], v[48:49] op_sel_hi:[1,0,1]
	v_pk_fma_f32 v[46:47], v[164:165], v[8:9], v[46:47] op_sel:[0,1,0]
	v_pk_fma_f32 v[48:49], v[164:165], v[16:17], v[48:49] op_sel:[0,1,0]
	s_nop 0
	v_add_f32_dpp v46, v46, v46 quad_perm:[1,0,3,2] row_mask:0xf bank_mask:0xf bound_ctrl:1
	v_add_f32_dpp v47, v47, v47 quad_perm:[1,0,3,2] row_mask:0xf bank_mask:0xf bound_ctrl:1
	v_add_f32_dpp v48, v48, v48 quad_perm:[1,0,3,2] row_mask:0xf bank_mask:0xf bound_ctrl:1
	v_add_f32_dpp v49, v49, v49 quad_perm:[1,0,3,2] row_mask:0xf bank_mask:0xf bound_ctrl:1
	v_add_f32_dpp v46, v46, v46 quad_perm:[2,3,0,1] row_mask:0xf bank_mask:0xf bound_ctrl:1
	v_add_f32_dpp v47, v47, v47 quad_perm:[2,3,0,1] row_mask:0xf bank_mask:0xf bound_ctrl:1
	v_add_f32_dpp v48, v48, v48 quad_perm:[2,3,0,1] row_mask:0xf bank_mask:0xf bound_ctrl:1
	v_add_f32_dpp v49, v49, v49 quad_perm:[2,3,0,1] row_mask:0xf bank_mask:0xf bound_ctrl:1
	v_add_f32_dpp v46, v46, v46 row_half_mirror row_mask:0xf bank_mask:0xf bound_ctrl:1
	v_add_f32_dpp v47, v47, v47 row_half_mirror row_mask:0xf bank_mask:0xf bound_ctrl:1
	v_add_f32_dpp v48, v48, v48 row_half_mirror row_mask:0xf bank_mask:0xf bound_ctrl:1
	v_add_f32_dpp v49, v49, v49 row_half_mirror row_mask:0xf bank_mask:0xf bound_ctrl:1
	v_pk_fma_f32 v[48:49], v[46:47], v[44:45], v[48:49] op_sel_hi:[1,0,1]
	v_pk_fma_f32 v[48:49], v[42:43], v[44:45], v[48:49] op_sel:[0,1,0]
	s_mov_b64 exec, s[100:101]
	ds_write_b64 v53, v[48:49] offset:768
	s_mov_b64 exec, -1
	v_pk_mul_f32 v[150:151], v[150:151], v[18:19] op_sel_hi:[1,0]
	v_pk_mul_f32 v[152:153], v[152:153], v[18:19] op_sel:[0,1]
	v_pk_mul_f32 v[154:155], v[154:155], v[20:21] op_sel_hi:[1,0]
	v_pk_mul_f32 v[156:157], v[156:157], v[20:21] op_sel:[0,1]
	v_pk_mul_f32 v[158:159], v[158:159], v[22:23] op_sel_hi:[1,0]
	v_pk_mul_f32 v[160:161], v[160:161], v[22:23] op_sel:[0,1]
	v_pk_mul_f32 v[162:163], v[162:163], v[24:25] op_sel_hi:[1,0]
	v_pk_mul_f32 v[164:165], v[164:165], v[24:25] op_sel:[0,1]
	v_pk_fma_f32 v[150:151], v[46:47], v[26:27], v[150:151] op_sel_hi:[1,0,1]
	v_pk_fma_f32 v[152:153], v[46:47], v[26:27], v[152:153] op_sel:[0,1,0]
	v_pk_fma_f32 v[154:155], v[46:47], v[28:29], v[154:155] op_sel_hi:[1,0,1]
	v_pk_fma_f32 v[156:157], v[46:47], v[28:29], v[156:157] op_sel:[0,1,0]
	v_pk_fma_f32 v[158:159], v[46:47], v[30:31], v[158:159] op_sel_hi:[1,0,1]
	v_pk_fma_f32 v[160:161], v[46:47], v[30:31], v[160:161] op_sel:[0,1,0]
	v_pk_fma_f32 v[162:163], v[46:47], v[32:33], v[162:163] op_sel_hi:[1,0,1]
	v_pk_fma_f32 v[164:165], v[46:47], v[32:33], v[164:165] op_sel:[0,1,0]
	v_pk_fma_f32 v[150:151], v[42:43], v[34:35], v[150:151] op_sel_hi:[1,0,1]
	v_pk_fma_f32 v[152:153], v[42:43], v[34:35], v[152:153] op_sel:[0,1,0]
	v_pk_fma_f32 v[154:155], v[42:43], v[36:37], v[154:155] op_sel_hi:[1,0,1]
	v_pk_fma_f32 v[156:157], v[42:43], v[36:37], v[156:157] op_sel:[0,1,0]
	v_pk_fma_f32 v[158:159], v[42:43], v[38:39], v[158:159] op_sel_hi:[1,0,1]
	v_pk_fma_f32 v[160:161], v[42:43], v[38:39], v[160:161] op_sel:[0,1,0]
	v_pk_fma_f32 v[162:163], v[42:43], v[40:41], v[162:163] op_sel_hi:[1,0,1]
	v_pk_fma_f32 v[164:165], v[42:43], v[40:41], v[164:165] op_sel:[0,1,0]
	s_waitcnt lgkmcnt(0)
; template <class AT_>
; __device__ __forceinline__ void rwkv_scan_phase(const AT_& a, Frame& F, int j) {
;     ...
;                     auto step = [&](const RwOps& cur, int t) {
;                         const f32x2 a01 = {cur.a0.x, cur.a0.y}, a23 = {cur.a0.z, cur.a0.w}, a45 = {cur.a1.x, cur.a1.y}, a67 = {cur.a1.z, cur.a1.w};
;                         const f32x2 r01 = {cur.r0.x, cur.r0.y}, r23 = {cur.r0.z, cur.r0.w}, r45 = {cur.r1.x, cur.r1.y}, r67 = {cur.r1.z, cur.r1.w};
;                         f32x2 sA0 = S0[0] * a01, sA1 = S1[0] * a01, sY0 = S0[0] * r01, sY1 = S1[0] * r01;
;                         sA0 = S0[1] * a23 + sA0; sA1 = S1[1] * a23 + sA1; sY0 = S0[1] * r23 + sY0; sY1 = S1[1] * r23 + sY1;
;                         sA0 = S0[2] * a45 + sA0; sA1 = S1[2] * a45 + sA1; sY0 = S0[2] * r45 + sY0; sY1 = S1[2] * r45 + sY1;
;                         sA0 = S0[3] * a67 + sA0; sA1 = S1[3] * a67 + sA1; sY0 = S0[3] * r67 + sY0; sY1 = S1[3] * r67 + sY1;
;                         const float sa0 = row8_allsum(sA0.x + sA0.y), sa1 = row8_allsum(sA1.x + sA1.y), yy0 = row8_allsum(sY0.x + sY0.y), yy1 = row8_allsum(sY1.x + sY1.y);
;                         if (kg == 0) { f32x2 yo; yo.x = yy0 + sa0 * cur.sc.x + cur.v.x * cur.sc.y; yo.y = yy1 + sa1 * cur.sc.x + cur.v.y * cur.sc.y; *(LAS f32x2*)(Yb + t * 64 + v0) = yo; }
;                         const f32x2 w01 = {cur.w0.x, cur.w0.y}, w23 = {cur.w0.z, cur.w0.w}, w45 = {cur.w1.x, cur.w1.y}, w67 = {cur.w1.z, cur.w1.w};
;                         const f32x2 b01 = {cur.b0.x, cur.b0.y}, b23 = {cur.b0.z, cur.b0.w}, b45 = {cur.b1.x, cur.b1.y}, b67 = {cur.b1.z, cur.b1.w};
;                         const f32x2 k01 = {cur.k0.x, cur.k0.y}, k23 = {cur.k0.z, cur.k0.w}, k45 = {cur.k1.x, cur.k1.y}, k67 = {cur.k1.z, cur.k1.w};
;                         const f32x2 s0 = {sa0, sa0}, s1 = {sa1, sa1}, x0 = {cur.v.x, cur.v.x}, x1 = {cur.v.y, cur.v.y};
;                         S0[0] = S0[0] * w01 + (s0 * b01 + x0 * k01); S0[1] = S0[1] * w23 + (s0 * b23 + x0 * k23); S0[2] = S0[2] * w45 + (s0 * b45 + x0 * k45); S0[3] = S0[3] * w67 + (s0 * b67 + x0 * k67);
;                         S1[0] = S1[0] * w01 + (s1 * b01 + x1 * k01); S1[1] = S1[1] * w23 + (s1 * b23 + x1 * k23); S1[2] = S1[2] * w45 + (s1 * b45 + x1 * k45); S1[3] = S1[3] * w67 + (s1 * b67 + x1 * k67);
;                     };
;                     RwOps oa = ld(0);
	ds_read_b128 v[2:5], v50 offset:1280
	ds_read_b128 v[6:9], v50 offset:1296
	ds_read_b128 v[10:13], v50 offset:9472
	ds_read_b128 v[14:17], v50 offset:9488
	ds_read_b128 v[18:21], v50 offset:17664
	ds_read_b128 v[22:25], v50 offset:17680
	ds_read_b128 v[26:29], v50 offset:25856
	ds_read_b128 v[30:33], v50 offset:25872
	ds_read_b128 v[34:37], v50 offset:34048
	ds_read_b128 v[38:41], v50 offset:34064
	ds_read_b64 v[42:43], v51 offset:42240
	ds_read_b64 v[44:45], v52 offset:49232
	v_pk_mul_f32 v[46:47], v[150:151], v[168:169] op_sel_hi:[1,0]
	v_pk_mul_f32 v[48:49], v[150:151], v[176:177] op_sel_hi:[1,0]
	v_pk_fma_f32 v[46:47], v[152:153], v[168:169], v[46:47] op_sel:[0,1,0]
	v_pk_fma_f32 v[48:49], v[152:153], v[176:177], v[48:49] op_sel:[0,1,0]
	v_pk_fma_f32 v[46:47], v[154:155], v[170:171], v[46:47] op_sel_hi:[1,0,1]
	v_pk_fma_f32 v[48:49], v[154:155], v[178:179], v[48:49] op_sel_hi:[1,0,1]
	v_pk_fma_f32 v[46:47], v[156:157], v[170:171], v[46:47] op_sel:[0,1,0]
	v_pk_fma_f32 v[48:49], v[156:157], v[178:179], v[48:49] op_sel:[0,1,0]
	v_pk_fma_f32 v[46:47], v[158:159], v[172:173], v[46:47] op_sel_hi:[1,0,1]
	v_pk_fma_f32 v[48:49], v[158:159], v[180:181], v[48:49] op_sel_hi:[1,0,1]
	v_pk_fma_f32 v[46:47], v[160:161], v[172:173], v[46:47] op_sel:[0,1,0]
	v_pk_fma_f32 v[48:49], v[160:161], v[180:181], v[48:49] op_sel:[0,1,0]
	v_pk_fma_f32 v[46:47], v[162:163], v[174:175], v[46:47] op_sel_hi:[1,0,1]
	v_pk_fma_f32 v[48:49], v[162:163], v[182:183], v[48:49] op_sel_hi:[1,0,1]
	v_pk_fma_f32 v[46:47], v[164:165], v[174:175], v[46:47] op_sel:[0,1,0]
	v_pk_fma_f32 v[48:49], v[164:165], v[182:183], v[48:49] op_sel:[0,1,0]
	s_nop 0
	v_add_f32_dpp v46, v46, v46 quad_perm:[1,0,3,2] row_mask:0xf bank_mask:0xf bound_ctrl:1
	v_add_f32_dpp v47, v47, v47 quad_perm:[1,0,3,2] row_mask:0xf bank_mask:0xf bound_ctrl:1
	v_add_f32_dpp v48, v48, v48 quad_perm:[1,0,3,2] row_mask:0xf bank_mask:0xf bound_ctrl:1
	v_add_f32_dpp v49, v49, v49 quad_perm:[1,0,3,2] row_mask:0xf bank_mask:0xf bound_ctrl:1
	v_add_f32_dpp v46, v46, v46 quad_perm:[2,3,0,1] row_mask:0xf bank_mask:0xf bound_ctrl:1
	v_add_f32_dpp v47, v47, v47 quad_perm:[2,3,0,1] row_mask:0xf bank_mask:0xf bound_ctrl:1
	v_add_f32_dpp v48, v48, v48 quad_perm:[2,3,0,1] row_mask:0xf bank_mask:0xf bound_ctrl:1
	v_add_f32_dpp v49, v49, v49 quad_perm:[2,3,0,1] row_mask:0xf bank_mask:0xf bound_ctrl:1
	v_add_f32_dpp v46, v46, v46 row_half_mirror row_mask:0xf bank_mask:0xf bound_ctrl:1
	v_add_f32_dpp v47, v47, v47 row_half_mirror row_mask:0xf bank_mask:0xf bound_ctrl:1
	v_add_f32_dpp v48, v48, v48 row_half_mirror row_mask:0xf bank_mask:0xf bound_ctrl:1
	v_add_f32_dpp v49, v49, v49 row_half_mirror row_mask:0xf bank_mask:0xf bound_ctrl:1
	v_pk_fma_f32 v[48:49], v[46:47], v[210:211], v[48:49] op_sel_hi:[1,0,1]
	v_pk_fma_f32 v[48:49], v[208:209], v[210:211], v[48:49] op_sel:[0,1,0]
	s_mov_b64 exec, s[100:101]
	ds_write_b64 v53, v[48:49] offset:1024
	s_mov_b64 exec, -1
	v_pk_mul_f32 v[150:151], v[150:151], v[184:185] op_sel_hi:[1,0]
	v_pk_mul_f32 v[152:153], v[152:153], v[184:185] op_sel:[0,1]
	v_pk_mul_f32 v[154:155], v[154:155], v[186:187] op_sel_hi:[1,0]
	v_pk_mul_f32 v[156:157], v[156:157], v[186:187] op_sel:[0,1]
	v_pk_mul_f32 v[158:159], v[158:159], v[188:189] op_sel_hi:[1,0]
	v_pk_mul_f32 v[160:161], v[160:161], v[188:189] op_sel:[0,1]
	v_pk_mul_f32 v[162:163], v[162:163], v[190:191] op_sel_hi:[1,0]
	v_pk_mul_f32 v[164:165], v[164:165], v[190:191] op_sel:[0,1]
	v_pk_fma_f32 v[150:151], v[46:47], v[192:193], v[150:151] op_sel_hi:[1,0,1]
	v_pk_fma_f32 v[152:153], v[46:47], v[192:193], v[152:153] op_sel:[0,1,0]
	v_pk_fma_f32 v[154:155], v[46:47], v[194:195], v[154:155] op_sel_hi:[1,0,1]
	v_pk_fma_f32 v[156:157], v[46:47], v[194:195], v[156:157] op_sel:[0,1,0]
	v_pk_fma_f32 v[158:159], v[46:47], v[196:197], v[158:159] op_sel_hi:[1,0,1]
	v_pk_fma_f32 v[160:161], v[46:47], v[196:197], v[160:161] op_sel:[0,1,0]
	v_pk_fma_f32 v[162:163], v[46:47], v[198:199], v[162:163] op_sel_hi:[1,0,1]
	v_pk_fma_f32 v[164:165], v[46:47], v[198:199], v[164:165] op_sel:[0,1,0]
	v_pk_fma_f32 v[150:151], v[208:209], v[200:201], v[150:151] op_sel_hi:[1,0,1]
	v_pk_fma_f32 v[152:153], v[208:209], v[200:201], v[152:153] op_sel:[0,1,0]
	v_pk_fma_f32 v[154:155], v[208:209], v[202:203], v[154:155] op_sel_hi:[1,0,1]
	v_pk_fma_f32 v[156:157], v[208:209], v[202:203], v[156:157] op_sel:[0,1,0]
	v_pk_fma_f32 v[158:159], v[208:209], v[204:205], v[158:159] op_sel_hi:[1,0,1]
	v_pk_fma_f32 v[160:161], v[208:209], v[204:205], v[160:161] op_sel:[0,1,0]
	v_pk_fma_f32 v[162:163], v[208:209], v[206:207], v[162:163] op_sel_hi:[1,0,1]
	v_pk_fma_f32 v[164:165], v[208:209], v[206:207], v[164:165] op_sel:[0,1,0]
	s_waitcnt lgkmcnt(0)
; template <class AT_>
; __device__ __forceinline__ void rwkv_scan_phase(const AT_& a, Frame& F, int j) {
;     ...
;                     auto step = [&](const RwOps& cur, int t) {
;                         const f32x2 a01 = {cur.a0.x, cur.a0.y}, a23 = {cur.a0.z, cur.a0.w}, a45 = {cur.a1.x, cur.a1.y}, a67 = {cur.a1.z, cur.a1.w};
;                         const f32x2 r01 = {cur.r0.x, cur.r0.y}, r23 = {cur.r0.z, cur.r0.w}, r45 = {cur.r1.x, cur.r1.y}, r67 = {cur.r1.z, cur.r1.w};
;                         f32x2 sA0 = S0[0] * a01, sA1 = S1[0] * a01, sY0 = S0[0] * r01, sY1 = S1[0] * r01;
;                         sA0 = S0[1] * a23 + sA0; sA1 = S1[1] * a23 + sA1; sY0 = S0[1] * r23 + sY0; sY1 = S1[1] * r23 + sY1;
;                         sA0 = S0[2] * a45 + sA0; sA1 = S1[2] * a45 + sA1; sY0 = S0[2] * r45 + sY0; sY1 = S1[2] * r45 + sY1;
;                         sA0 = S0[3] * a67 + sA0; sA1 = S1[3] * a67 + sA1; sY0 = S0[3] * r67 + sY0; sY1 = S1[3] * r67 + sY1;
;                         const float sa0 = row8_allsum(sA0.x + sA0.y), sa1 = row8_allsum(sA1.x + sA1.y), yy0 = row8_allsum(sY0.x + sY0.y), yy1 = row8_allsum(sY1.x + sY1.y);
;                         if (kg == 0) { f32x2 yo; yo.x = yy0 + sa0 * cur.sc.x + cur.v.x * cur.sc.y; yo.y = yy1 + sa1 * cur.sc.x + cur.v.y * cur.sc.y; *(LAS f32x2*)(Yb + t * 64 + v0) = yo; }
;                         const f32x2 w01 = {cur.w0.x, cur.w0.y}, w23 = {cur.w0.z, cur.w0.w}, w45 = {cur.w1.x, cur.w1.y}, w67 = {cur.w1.z, cur.w1.w};
;                         const f32x2 b01 = {cur.b0.x, cur.b0.y}, b23 = {cur.b0.z, cur.b0.w}, b45 = {cur.b1.x, cur.b1.y}, b67 = {cur.b1.z, cur.b1.w};
;                         const f32x2 k01 = {cur.k0.x, cur.k0.y}, k23 = {cur.k0.z, cur.k0.w}, k45 = {cur.k1.x, cur.k1.y}, k67 = {cur.k1.z, cur.k1.w};
;                         const f32x2 s0 = {sa0, sa0}, s1 = {sa1, sa1}, x0 = {cur.v.x, cur.v.x}, x1 = {cur.v.y, cur.v.y};
;                         S0[0] = S0[0] * w01 + (s0 * b01 + x0 * k01); S0[1] = S0[1] * w23 + (s0 * b23 + x0 * k23); S0[2] = S0[2] * w45 + (s0 * b45 + x0 * k45); S0[3] = S0[3] * w67 + (s0 * b67 + x0 * k67);
;                         S1[0] = S1[0] * w01 + (s1 * b01 + x1 * k01); S1[1] = S1[1] * w23 + (s1 * b23 + x1 * k23); S1[2] = S1[2] * w45 + (s1 * b45 + x1 * k45); S1[3] = S1[3] * w67 + (s1 * b67 + x1 * k67);
;                     };
;                     RwOps oa = ld(0);
	ds_read_b128 v[168:171], v50 offset:1536
	ds_read_b128 v[172:175], v50 offset:1552
	ds_read_b128 v[176:179], v50 offset:9728
	ds_read_b128 v[180:183], v50 offset:9744
	ds_read_b128 v[184:187], v50 offset:17920
	ds_read_b128 v[188:191], v50 offset:17936
	ds_read_b128 v[192:195], v50 offset:26112
	ds_read_b128 v[196:199], v50 offset:26128
	ds_read_b128 v[200:203], v50 offset:34304
	ds_read_b128 v[204:207], v50 offset:34320
	ds_read_b64 v[208:209], v51 offset:42496
	ds_read_b64 v[210:211], v52 offset:49248
	v_pk_mul_f32 v[46:47], v[150:151], v[2:3] op_sel_hi:[1,0]
	v_pk_mul_f32 v[48:49], v[150:151], v[10:11] op_sel_hi:[1,0]
	v_pk_fma_f32 v[46:47], v[152:153], v[2:3], v[46:47] op_sel:[0,1,0]
	v_pk_fma_f32 v[48:49], v[152:153], v[10:11], v[48:49] op_sel:[0,1,0]
	v_pk_fma_f32 v[46:47], v[154:155], v[4:5], v[46:47] op_sel_hi:[1,0,1]
	v_pk_fma_f32 v[48:49], v[154:155], v[12:13], v[48:49] op_sel_hi:[1,0,1]
	v_pk_fma_f32 v[46:47], v[156:157], v[4:5], v[46:47] op_sel:[0,1,0]
	v_pk_fma_f32 v[48:49], v[156:157], v[12:13], v[48:49] op_sel:[0,1,0]
	v_pk_fma_f32 v[46:47], v[158:159], v[6:7], v[46:47] op_sel_hi:[1,0,1]
	v_pk_fma_f32 v[48:49], v[158:159], v[14:15], v[48:49] op_sel_hi:[1,0,1]
	v_pk_fma_f32 v[46:47], v[160:161], v[6:7], v[46:47] op_sel:[0,1,0]
	v_pk_fma_f32 v[48:49], v[160:161], v[14:15], v[48:49] op_sel:[0,1,0]
	v_pk_fma_f32 v[46:47], v[162:163], v[8:9], v[46:47] op_sel_hi:[1,0,1]
	v_pk_fma_f32 v[48:49], v[162:163], v[16:17], v[48:49] op_sel_hi:[1,0,1]
	v_pk_fma_f32 v[46:47], v[164:165], v[8:9], v[46:47] op_sel:[0,1,0]
	v_pk_fma_f32 v[48:49], v[164:165], v[16:17], v[48:49] op_sel:[0,1,0]
	s_nop 0
	v_add_f32_dpp v46, v46, v46 quad_perm:[1,0,3,2] row_mask:0xf bank_mask:0xf bound_ctrl:1
	v_add_f32_dpp v47, v47, v47 quad_perm:[1,0,3,2] row_mask:0xf bank_mask:0xf bound_ctrl:1
	v_add_f32_dpp v48, v48, v48 quad_perm:[1,0,3,2] row_mask:0xf bank_mask:0xf bound_ctrl:1
	v_add_f32_dpp v49, v49, v49 quad_perm:[1,0,3,2] row_mask:0xf bank_mask:0xf bound_ctrl:1
	v_add_f32_dpp v46, v46, v46 quad_perm:[2,3,0,1] row_mask:0xf bank_mask:0xf bound_ctrl:1
	v_add_f32_dpp v47, v47, v47 quad_perm:[2,3,0,1] row_mask:0xf bank_mask:0xf bound_ctrl:1
	v_add_f32_dpp v48, v48, v48 quad_perm:[2,3,0,1] row_mask:0xf bank_mask:0xf bound_ctrl:1
	v_add_f32_dpp v49, v49, v49 quad_perm:[2,3,0,1] row_mask:0xf bank_mask:0xf bound_ctrl:1
	v_add_f32_dpp v46, v46, v46 row_half_mirror row_mask:0xf bank_mask:0xf bound_ctrl:1
	v_add_f32_dpp v47, v47, v47 row_half_mirror row_mask:0xf bank_mask:0xf bound_ctrl:1
	v_add_f32_dpp v48, v48, v48 row_half_mirror row_mask:0xf bank_mask:0xf bound_ctrl:1
	v_add_f32_dpp v49, v49, v49 row_half_mirror row_mask:0xf bank_mask:0xf bound_ctrl:1
	v_pk_fma_f32 v[48:49], v[46:47], v[44:45], v[48:49] op_sel_hi:[1,0,1]
	v_pk_fma_f32 v[48:49], v[42:43], v[44:45], v[48:49] op_sel:[0,1,0]
	s_mov_b64 exec, s[100:101]
	ds_write_b64 v53, v[48:49] offset:1280
	s_mov_b64 exec, -1
	v_pk_mul_f32 v[150:151], v[150:151], v[18:19] op_sel_hi:[1,0]
	v_pk_mul_f32 v[152:153], v[152:153], v[18:19] op_sel:[0,1]
	v_pk_mul_f32 v[154:155], v[154:155], v[20:21] op_sel_hi:[1,0]
	v_pk_mul_f32 v[156:157], v[156:157], v[20:21] op_sel:[0,1]
	v_pk_mul_f32 v[158:159], v[158:159], v[22:23] op_sel_hi:[1,0]
	v_pk_mul_f32 v[160:161], v[160:161], v[22:23] op_sel:[0,1]
	v_pk_mul_f32 v[162:163], v[162:163], v[24:25] op_sel_hi:[1,0]
	v_pk_mul_f32 v[164:165], v[164:165], v[24:25] op_sel:[0,1]
	v_pk_fma_f32 v[150:151], v[46:47], v[26:27], v[150:151] op_sel_hi:[1,0,1]
	v_pk_fma_f32 v[152:153], v[46:47], v[26:27], v[152:153] op_sel:[0,1,0]
	v_pk_fma_f32 v[154:155], v[46:47], v[28:29], v[154:155] op_sel_hi:[1,0,1]
	v_pk_fma_f32 v[156:157], v[46:47], v[28:29], v[156:157] op_sel:[0,1,0]
	v_pk_fma_f32 v[158:159], v[46:47], v[30:31], v[158:159] op_sel_hi:[1,0,1]
	v_pk_fma_f32 v[160:161], v[46:47], v[30:31], v[160:161] op_sel:[0,1,0]
	v_pk_fma_f32 v[162:163], v[46:47], v[32:33], v[162:163] op_sel_hi:[1,0,1]
	v_pk_fma_f32 v[164:165], v[46:47], v[32:33], v[164:165] op_sel:[0,1,0]
	v_pk_fma_f32 v[150:151], v[42:43], v[34:35], v[150:151] op_sel_hi:[1,0,1]
	v_pk_fma_f32 v[152:153], v[42:43], v[34:35], v[152:153] op_sel:[0,1,0]
	v_pk_fma_f32 v[154:155], v[42:43], v[36:37], v[154:155] op_sel_hi:[1,0,1]
	v_pk_fma_f32 v[156:157], v[42:43], v[36:37], v[156:157] op_sel:[0,1,0]
	v_pk_fma_f32 v[158:159], v[42:43], v[38:39], v[158:159] op_sel_hi:[1,0,1]
	v_pk_fma_f32 v[160:161], v[42:43], v[38:39], v[160:161] op_sel:[0,1,0]
	v_pk_fma_f32 v[162:163], v[42:43], v[40:41], v[162:163] op_sel_hi:[1,0,1]
	v_pk_fma_f32 v[164:165], v[42:43], v[40:41], v[164:165] op_sel:[0,1,0]
	s_waitcnt lgkmcnt(0)
; template <class AT_>
; __device__ __forceinline__ void rwkv_scan_phase(const AT_& a, Frame& F, int j) {
;     ...
;                     auto step = [&](const RwOps& cur, int t) {
;                         const f32x2 a01 = {cur.a0.x, cur.a0.y}, a23 = {cur.a0.z, cur.a0.w}, a45 = {cur.a1.x, cur.a1.y}, a67 = {cur.a1.z, cur.a1.w};
;                         const f32x2 r01 = {cur.r0.x, cur.r0.y}, r23 = {cur.r0.z, cur.r0.w}, r45 = {cur.r1.x, cur.r1.y}, r67 = {cur.r1.z, cur.r1.w};
;                         f32x2 sA0 = S0[0] * a01, sA1 = S1[0] * a01, sY0 = S0[0] * r01, sY1 = S1[0] * r01;
;                         sA0 = S0[1] * a23 + sA0; sA1 = S1[1] * a23 + sA1; sY0 = S0[1] * r23 + sY0; sY1 = S1[1] * r23 + sY1;
;                         sA0 = S0[2] * a45 + sA0; sA1 = S1[2] * a45 + sA1; sY0 = S0[2] * r45 + sY0; sY1 = S1[2] * r45 + sY1;
;                         sA0 = S0[3] * a67 + sA0; sA1 = S1[3] * a67 + sA1; sY0 = S0[3] * r67 + sY0; sY1 = S1[3] * r67 + sY1;
;                         const float sa0 = row8_allsum(sA0.x + sA0.y), sa1 = row8_allsum(sA1.x + sA1.y), yy0 = row8_allsum(sY0.x + sY0.y), yy1 = row8_allsum(sY1.x + sY1.y);
;                         if (kg == 0) { f32x2 yo; yo.x = yy0 + sa0 * cur.sc.x + cur.v.x * cur.sc.y; yo.y = yy1 + sa1 * cur.sc.x + cur.v.y * cur.sc.y; *(LAS f32x2*)(Yb + t * 64 + v0) = yo; }
;                         const f32x2 w01 = {cur.w0.x, cur.w0.y}, w23 = {cur.w0.z, cur.w0.w}, w45 = {cur.w1.x, cur.w1.y}, w67 = {cur.w1.z, cur.w1.w};
;                         const f32x2 b01 = {cur.b0.x, cur.b0.y}, b23 = {cur.b0.z, cur.b0.w}, b45 = {cur.b1.x, cur.b1.y}, b67 = {cur.b1.z, cur.b1.w};
;                         const f32x2 k01 = {cur.k0.x, cur.k0.y}, k23 = {cur.k0.z, cur.k0.w}, k45 = {cur.k1.x, cur.k1.y}, k67 = {cur.k1.z, cur.k1.w};
;                         const f32x2 s0 = {sa0, sa0}, s1 = {sa1, sa1}, x0 = {cur.v.x, cur.v.x}, x1 = {cur.v.y, cur.v.y};
;                         S0[0] = S0[0] * w01 + (s0 * b01 + x0 * k01); S0[1] = S0[1] * w23 + (s0 * b23 + x0 * k23); S0[2] = S0[2] * w45 + (s0 * b45 + x0 * k45); S0[3] = S0[3] * w67 + (s0 * b67 + x0 * k67);
;                         S1[0] = S1[0] * w01 + (s1 * b01 + x1 * k01); S1[1] = S1[1] * w23 + (s1 * b23 + x1 * k23); S1[2] = S1[2] * w45 + (s1 * b45 + x1 * k45); S1[3] = S1[3] * w67 + (s1 * b67 + x1 * k67);
;                     };
;                     RwOps oa = ld(0);
	ds_read_b128 v[2:5], v50 offset:1792
	ds_read_b128 v[6:9], v50 offset:1808
	ds_read_b128 v[10:13], v50 offset:9984
	ds_read_b128 v[14:17], v50 offset:10000
	ds_read_b128 v[18:21], v50 offset:18176
	ds_read_b128 v[22:25], v50 offset:18192
	ds_read_b128 v[26:29], v50 offset:26368
	ds_read_b128 v[30:33], v50 offset:26384
	ds_read_b128 v[34:37], v50 offset:34560
	ds_read_b128 v[38:41], v50 offset:34576
	ds_read_b64 v[42:43], v51 offset:42752
	ds_read_b64 v[44:45], v52 offset:49264
	v_pk_mul_f32 v[46:47], v[150:151], v[168:169] op_sel_hi:[1,0]
	v_pk_mul_f32 v[48:49], v[150:151], v[176:177] op_sel_hi:[1,0]
	v_pk_fma_f32 v[46:47], v[152:153], v[168:169], v[46:47] op_sel:[0,1,0]
	v_pk_fma_f32 v[48:49], v[152:153], v[176:177], v[48:49] op_sel:[0,1,0]
	v_pk_fma_f32 v[46:47], v[154:155], v[170:171], v[46:47] op_sel_hi:[1,0,1]
	v_pk_fma_f32 v[48:49], v[154:155], v[178:179], v[48:49] op_sel_hi:[1,0,1]
	v_pk_fma_f32 v[46:47], v[156:157], v[170:171], v[46:47] op_sel:[0,1,0]
	v_pk_fma_f32 v[48:49], v[156:157], v[178:179], v[48:49] op_sel:[0,1,0]
	v_pk_fma_f32 v[46:47], v[158:159], v[172:173], v[46:47] op_sel_hi:[1,0,1]
	v_pk_fma_f32 v[48:49], v[158:159], v[180:181], v[48:49] op_sel_hi:[1,0,1]
	v_pk_fma_f32 v[46:47], v[160:161], v[172:173], v[46:47] op_sel:[0,1,0]
	v_pk_fma_f32 v[48:49], v[160:161], v[180:181], v[48:49] op_sel:[0,1,0]
	v_pk_fma_f32 v[46:47], v[162:163], v[174:175], v[46:47] op_sel_hi:[1,0,1]
	v_pk_fma_f32 v[48:49], v[162:163], v[182:183], v[48:49] op_sel_hi:[1,0,1]
	v_pk_fma_f32 v[46:47], v[164:165], v[174:175], v[46:47] op_sel:[0,1,0]
	v_pk_fma_f32 v[48:49], v[164:165], v[182:183], v[48:49] op_sel:[0,1,0]
	s_nop 0
	v_add_f32_dpp v46, v46, v46 quad_perm:[1,0,3,2] row_mask:0xf bank_mask:0xf bound_ctrl:1
	v_add_f32_dpp v47, v47, v47 quad_perm:[1,0,3,2] row_mask:0xf bank_mask:0xf bound_ctrl:1
	v_add_f32_dpp v48, v48, v48 quad_perm:[1,0,3,2] row_mask:0xf bank_mask:0xf bound_ctrl:1
	v_add_f32_dpp v49, v49, v49 quad_perm:[1,0,3,2] row_mask:0xf bank_mask:0xf bound_ctrl:1
	v_add_f32_dpp v46, v46, v46 quad_perm:[2,3,0,1] row_mask:0xf bank_mask:0xf bound_ctrl:1
	v_add_f32_dpp v47, v47, v47 quad_perm:[2,3,0,1] row_mask:0xf bank_mask:0xf bound_ctrl:1
	v_add_f32_dpp v48, v48, v48 quad_perm:[2,3,0,1] row_mask:0xf bank_mask:0xf bound_ctrl:1
	v_add_f32_dpp v49, v49, v49 quad_perm:[2,3,0,1] row_mask:0xf bank_mask:0xf bound_ctrl:1
	v_add_f32_dpp v46, v46, v46 row_half_mirror row_mask:0xf bank_mask:0xf bound_ctrl:1
	v_add_f32_dpp v47, v47, v47 row_half_mirror row_mask:0xf bank_mask:0xf bound_ctrl:1
	v_add_f32_dpp v48, v48, v48 row_half_mirror row_mask:0xf bank_mask:0xf bound_ctrl:1
	v_add_f32_dpp v49, v49, v49 row_half_mirror row_mask:0xf bank_mask:0xf bound_ctrl:1
	v_pk_fma_f32 v[48:49], v[46:47], v[210:211], v[48:49] op_sel_hi:[1,0,1]
	v_pk_fma_f32 v[48:49], v[208:209], v[210:211], v[48:49] op_sel:[0,1,0]
	s_mov_b64 exec, s[100:101]
	ds_write_b64 v53, v[48:49] offset:1536
	s_mov_b64 exec, -1
	v_pk_mul_f32 v[150:151], v[150:151], v[184:185] op_sel_hi:[1,0]
	v_pk_mul_f32 v[152:153], v[152:153], v[184:185] op_sel:[0,1]
	v_pk_mul_f32 v[154:155], v[154:155], v[186:187] op_sel_hi:[1,0]
	v_pk_mul_f32 v[156:157], v[156:157], v[186:187] op_sel:[0,1]
	v_pk_mul_f32 v[158:159], v[158:159], v[188:189] op_sel_hi:[1,0]
	v_pk_mul_f32 v[160:161], v[160:161], v[188:189] op_sel:[0,1]
	v_pk_mul_f32 v[162:163], v[162:163], v[190:191] op_sel_hi:[1,0]
	v_pk_mul_f32 v[164:165], v[164:165], v[190:191] op_sel:[0,1]
	v_pk_fma_f32 v[150:151], v[46:47], v[192:193], v[150:151] op_sel_hi:[1,0,1]
	v_pk_fma_f32 v[152:153], v[46:47], v[192:193], v[152:153] op_sel:[0,1,0]
	v_pk_fma_f32 v[154:155], v[46:47], v[194:195], v[154:155] op_sel_hi:[1,0,1]
	v_pk_fma_f32 v[156:157], v[46:47], v[194:195], v[156:157] op_sel:[0,1,0]
	v_pk_fma_f32 v[158:159], v[46:47], v[196:197], v[158:159] op_sel_hi:[1,0,1]
	v_pk_fma_f32 v[160:161], v[46:47], v[196:197], v[160:161] op_sel:[0,1,0]
	v_pk_fma_f32 v[162:163], v[46:47], v[198:199], v[162:163] op_sel_hi:[1,0,1]
	v_pk_fma_f32 v[164:165], v[46:47], v[198:199], v[164:165] op_sel:[0,1,0]
	v_pk_fma_f32 v[150:151], v[208:209], v[200:201], v[150:151] op_sel_hi:[1,0,1]
	v_pk_fma_f32 v[152:153], v[208:209], v[200:201], v[152:153] op_sel:[0,1,0]
	v_pk_fma_f32 v[154:155], v[208:209], v[202:203], v[154:155] op_sel_hi:[1,0,1]
	v_pk_fma_f32 v[156:157], v[208:209], v[202:203], v[156:157] op_sel:[0,1,0]
	v_pk_fma_f32 v[158:159], v[208:209], v[204:205], v[158:159] op_sel_hi:[1,0,1]
	v_pk_fma_f32 v[160:161], v[208:209], v[204:205], v[160:161] op_sel:[0,1,0]
	v_pk_fma_f32 v[162:163], v[208:209], v[206:207], v[162:163] op_sel_hi:[1,0,1]
	v_pk_fma_f32 v[164:165], v[208:209], v[206:207], v[164:165] op_sel:[0,1,0]
	s_waitcnt lgkmcnt(0)
; template <class AT_>
; __device__ __forceinline__ void rwkv_scan_phase(const AT_& a, Frame& F, int j) {
;     ...
;                     auto step = [&](const RwOps& cur, int t) {
;                         const f32x2 a01 = {cur.a0.x, cur.a0.y}, a23 = {cur.a0.z, cur.a0.w}, a45 = {cur.a1.x, cur.a1.y}, a67 = {cur.a1.z, cur.a1.w};
;                         const f32x2 r01 = {cur.r0.x, cur.r0.y}, r23 = {cur.r0.z, cur.r0.w}, r45 = {cur.r1.x, cur.r1.y}, r67 = {cur.r1.z, cur.r1.w};
;                         f32x2 sA0 = S0[0] * a01, sA1 = S1[0] * a01, sY0 = S0[0] * r01, sY1 = S1[0] * r01;
;                         sA0 = S0[1] * a23 + sA0; sA1 = S1[1] * a23 + sA1; sY0 = S0[1] * r23 + sY0; sY1 = S1[1] * r23 + sY1;
;                         sA0 = S0[2] * a45 + sA0; sA1 = S1[2] * a45 + sA1; sY0 = S0[2] * r45 + sY0; sY1 = S1[2] * r45 + sY1;
;                         sA0 = S0[3] * a67 + sA0; sA1 = S1[3] * a67 + sA1; sY0 = S0[3] * r67 + sY0; sY1 = S1[3] * r67 + sY1;
;                         const float sa0 = row8_allsum(sA0.x + sA0.y), sa1 = row8_allsum(sA1.x + sA1.y), yy0 = row8_allsum(sY0.x + sY0.y), yy1 = row8_allsum(sY1.x + sY1.y);
;                         if (kg == 0) { f32x2 yo; yo.x = yy0 + sa0 * cur.sc.x + cur.v.x * cur.sc.y; yo.y = yy1 + sa1 * cur.sc.x + cur.v.y * cur.sc.y; *(LAS f32x2*)(Yb + t * 64 + v0) = yo; }
;                         const f32x2 w01 = {cur.w0.x, cur.w0.y}, w23 = {cur.w0.z, cur.w0.w}, w45 = {cur.w1.x, cur.w1.y}, w67 = {cur.w1.z, cur.w1.w};
;                         const f32x2 b01 = {cur.b0.x, cur.b0.y}, b23 = {cur.b0.z, cur.b0.w}, b45 = {cur.b1.x, cur.b1.y}, b67 = {cur.b1.z, cur.b1.w};
;                         const f32x2 k01 = {cur.k0.x, cur.k0.y}, k23 = {cur.k0.z, cur.k0.w}, k45 = {cur.k1.x, cur.k1.y}, k67 = {cur.k1.z, cur.k1.w};
;                         const f32x2 s0 = {sa0, sa0}, s1 = {sa1, sa1}, x0 = {cur.v.x, cur.v.x}, x1 = {cur.v.y, cur.v.y};
;                         S0[0] = S0[0] * w01 + (s0 * b01 + x0 * k01); S0[1] = S0[1] * w23 + (s0 * b23 + x0 * k23); S0[2] = S0[2] * w45 + (s0 * b45 + x0 * k45); S0[3] = S0[3] * w67 + (s0 * b67 + x0 * k67);
;                         S1[0] = S1[0] * w01 + (s1 * b01 + x1 * k01); S1[1] = S1[1] * w23 + (s1 * b23 + x1 * k23); S1[2] = S1[2] * w45 + (s1 * b45 + x1 * k45); S1[3] = S1[3] * w67 + (s1 * b67 + x1 * k67);
;                     };
;                     RwOps oa = ld(0);
	ds_read_b128 v[168:171], v50 offset:2048
	ds_read_b128 v[172:175], v50 offset:2064
	ds_read_b128 v[176:179], v50 offset:10240
	ds_read_b128 v[180:183], v50 offset:10256
	ds_read_b128 v[184:187], v50 offset:18432
	ds_read_b128 v[188:191], v50 offset:18448
	ds_read_b128 v[192:195], v50 offset:26624
	ds_read_b128 v[196:199], v50 offset:26640
	ds_read_b128 v[200:203], v50 offset:34816
	ds_read_b128 v[204:207], v50 offset:34832
	ds_read_b64 v[208:209], v51 offset:43008
	ds_read_b64 v[210:211], v52 offset:49280
	v_pk_mul_f32 v[46:47], v[150:151], v[2:3] op_sel_hi:[1,0]
	v_pk_mul_f32 v[48:49], v[150:151], v[10:11] op_sel_hi:[1,0]
	v_pk_fma_f32 v[46:47], v[152:153], v[2:3], v[46:47] op_sel:[0,1,0]
	v_pk_fma_f32 v[48:49], v[152:153], v[10:11], v[48:49] op_sel:[0,1,0]
	v_pk_fma_f32 v[46:47], v[154:155], v[4:5], v[46:47] op_sel_hi:[1,0,1]
	v_pk_fma_f32 v[48:49], v[154:155], v[12:13], v[48:49] op_sel_hi:[1,0,1]
	v_pk_fma_f32 v[46:47], v[156:157], v[4:5], v[46:47] op_sel:[0,1,0]
	v_pk_fma_f32 v[48:49], v[156:157], v[12:13], v[48:49] op_sel:[0,1,0]
	v_pk_fma_f32 v[46:47], v[158:159], v[6:7], v[46:47] op_sel_hi:[1,0,1]
	v_pk_fma_f32 v[48:49], v[158:159], v[14:15], v[48:49] op_sel_hi:[1,0,1]
	v_pk_fma_f32 v[46:47], v[160:161], v[6:7], v[46:47] op_sel:[0,1,0]
	v_pk_fma_f32 v[48:49], v[160:161], v[14:15], v[48:49] op_sel:[0,1,0]
	v_pk_fma_f32 v[46:47], v[162:163], v[8:9], v[46:47] op_sel_hi:[1,0,1]
	v_pk_fma_f32 v[48:49], v[162:163], v[16:17], v[48:49] op_sel_hi:[1,0,1]
	v_pk_fma_f32 v[46:47], v[164:165], v[8:9], v[46:47] op_sel:[0,1,0]
	v_pk_fma_f32 v[48:49], v[164:165], v[16:17], v[48:49] op_sel:[0,1,0]
	s_nop 0
	v_add_f32_dpp v46, v46, v46 quad_perm:[1,0,3,2] row_mask:0xf bank_mask:0xf bound_ctrl:1
	v_add_f32_dpp v47, v47, v47 quad_perm:[1,0,3,2] row_mask:0xf bank_mask:0xf bound_ctrl:1
	v_add_f32_dpp v48, v48, v48 quad_perm:[1,0,3,2] row_mask:0xf bank_mask:0xf bound_ctrl:1
	v_add_f32_dpp v49, v49, v49 quad_perm:[1,0,3,2] row_mask:0xf bank_mask:0xf bound_ctrl:1
	v_add_f32_dpp v46, v46, v46 quad_perm:[2,3,0,1] row_mask:0xf bank_mask:0xf bound_ctrl:1
	v_add_f32_dpp v47, v47, v47 quad_perm:[2,3,0,1] row_mask:0xf bank_mask:0xf bound_ctrl:1
	v_add_f32_dpp v48, v48, v48 quad_perm:[2,3,0,1] row_mask:0xf bank_mask:0xf bound_ctrl:1
	v_add_f32_dpp v49, v49, v49 quad_perm:[2,3,0,1] row_mask:0xf bank_mask:0xf bound_ctrl:1
	v_add_f32_dpp v46, v46, v46 row_half_mirror row_mask:0xf bank_mask:0xf bound_ctrl:1
	v_add_f32_dpp v47, v47, v47 row_half_mirror row_mask:0xf bank_mask:0xf bound_ctrl:1
	v_add_f32_dpp v48, v48, v48 row_half_mirror row_mask:0xf bank_mask:0xf bound_ctrl:1
	v_add_f32_dpp v49, v49, v49 row_half_mirror row_mask:0xf bank_mask:0xf bound_ctrl:1
	v_pk_fma_f32 v[48:49], v[46:47], v[44:45], v[48:49] op_sel_hi:[1,0,1]
	v_pk_fma_f32 v[48:49], v[42:43], v[44:45], v[48:49] op_sel:[0,1,0]
	s_mov_b64 exec, s[100:101]
	ds_write_b64 v53, v[48:49] offset:1792
	s_mov_b64 exec, -1
	v_pk_mul_f32 v[150:151], v[150:151], v[18:19] op_sel_hi:[1,0]
	v_pk_mul_f32 v[152:153], v[152:153], v[18:19] op_sel:[0,1]
	v_pk_mul_f32 v[154:155], v[154:155], v[20:21] op_sel_hi:[1,0]
	v_pk_mul_f32 v[156:157], v[156:157], v[20:21] op_sel:[0,1]
	v_pk_mul_f32 v[158:159], v[158:159], v[22:23] op_sel_hi:[1,0]
	v_pk_mul_f32 v[160:161], v[160:161], v[22:23] op_sel:[0,1]
	v_pk_mul_f32 v[162:163], v[162:163], v[24:25] op_sel_hi:[1,0]
	v_pk_mul_f32 v[164:165], v[164:165], v[24:25] op_sel:[0,1]
	v_pk_fma_f32 v[150:151], v[46:47], v[26:27], v[150:151] op_sel_hi:[1,0,1]
	v_pk_fma_f32 v[152:153], v[46:47], v[26:27], v[152:153] op_sel:[0,1,0]
	v_pk_fma_f32 v[154:155], v[46:47], v[28:29], v[154:155] op_sel_hi:[1,0,1]
	v_pk_fma_f32 v[156:157], v[46:47], v[28:29], v[156:157] op_sel:[0,1,0]
	v_pk_fma_f32 v[158:159], v[46:47], v[30:31], v[158:159] op_sel_hi:[1,0,1]
	v_pk_fma_f32 v[160:161], v[46:47], v[30:31], v[160:161] op_sel:[0,1,0]
	v_pk_fma_f32 v[162:163], v[46:47], v[32:33], v[162:163] op_sel_hi:[1,0,1]
	v_pk_fma_f32 v[164:165], v[46:47], v[32:33], v[164:165] op_sel:[0,1,0]
	v_pk_fma_f32 v[150:151], v[42:43], v[34:35], v[150:151] op_sel_hi:[1,0,1]
	v_pk_fma_f32 v[152:153], v[42:43], v[34:35], v[152:153] op_sel:[0,1,0]
	v_pk_fma_f32 v[154:155], v[42:43], v[36:37], v[154:155] op_sel_hi:[1,0,1]
	v_pk_fma_f32 v[156:157], v[42:43], v[36:37], v[156:157] op_sel:[0,1,0]
	v_pk_fma_f32 v[158:159], v[42:43], v[38:39], v[158:159] op_sel_hi:[1,0,1]
	v_pk_fma_f32 v[160:161], v[42:43], v[38:39], v[160:161] op_sel:[0,1,0]
	v_pk_fma_f32 v[162:163], v[42:43], v[40:41], v[162:163] op_sel_hi:[1,0,1]
	v_pk_fma_f32 v[164:165], v[42:43], v[40:41], v[164:165] op_sel:[0,1,0]
	v_add_u32_e32 v50, 2048, v50
	v_add_u32_e32 v51, 2048, v51
	v_add_u32_e32 v52, 128, v52
	v_add_u32_e32 v53, 2048, v53
	s_sub_u32 s98, s98, 1
	s_cmp_lg_u32 s98, 0
	s_cbranch_scc1 .Lscan_a_loop
	s_branch .LBB0_3487

; __global__ void __launch_bounds__(NTHREADS, 2) hybrid_fwd(Args a_unused) {
	.amdhsa_kernel _Z10hybrid_fwd4Args
		.amdhsa_group_segment_fixed_size 0
		.amdhsa_private_segment_fixed_size 0
		.amdhsa_kernarg_size 552
		.amdhsa_user_sgpr_count 2
		.amdhsa_user_sgpr_dispatch_ptr 0
		.amdhsa_user_sgpr_queue_ptr 0
		.amdhsa_user_sgpr_kernarg_segment_ptr 1
		.amdhsa_user_sgpr_dispatch_id 0
		.amdhsa_user_sgpr_kernarg_preload_length 0
		.amdhsa_user_sgpr_kernarg_preload_offset 0
		.amdhsa_user_sgpr_private_segment_size 0
		.amdhsa_uses_dynamic_stack 0
		.amdhsa_enable_private_segment 0
		.amdhsa_system_sgpr_workgroup_id_x 1
		.amdhsa_system_sgpr_workgroup_id_y 0
		.amdhsa_system_sgpr_workgroup_id_z 0
		.amdhsa_system_sgpr_workgroup_info 0
		.amdhsa_system_vgpr_workitem_id 0
		.amdhsa_next_free_vgpr 248
		.amdhsa_next_free_sgpr 102
		.amdhsa_accum_offset 248
		.amdhsa_reserve_vcc 1
		.amdhsa_float_round_mode_32 0
		.amdhsa_float_round_mode_16_64 0
		.amdhsa_float_denorm_mode_32 3
		.amdhsa_float_denorm_mode_16_64 3
		.amdhsa_dx10_clamp 1
		.amdhsa_ieee_mode 1
		.amdhsa_fp16_overflow 0
		.amdhsa_tg_split 0
		.amdhsa_exception_fp_ieee_invalid_op 0
		.amdhsa_exception_fp_denorm_src 0
		.amdhsa_exception_fp_ieee_div_zero 0
		.amdhsa_exception_fp_ieee_overflow 0
		.amdhsa_exception_fp_ieee_underflow 0
		.amdhsa_exception_fp_ieee_inexact 0
		.amdhsa_exception_int_div_zero 0
	.end_amdhsa_kernel

; __global__ void __launch_bounds__(NTHREADS, 2) hybrid_fwd(Args a_unused) {
amdhsa.kernels:
  - .agpr_count:     0
    .args:
      - .offset:         0
        .size:           296
        .value_kind:     by_value
      - .offset:         296
        .size:           4
        .value_kind:     hidden_block_count_x
      - .offset:         300
        .size:           4
        .value_kind:     hidden_block_count_y
      - .offset:         304
        .size:           4
        .value_kind:     hidden_block_count_z
      - .offset:         308
        .size:           2
        .value_kind:     hidden_group_size_x
      - .offset:         310
        .size:           2
        .value_kind:     hidden_group_size_y
      - .offset:         312
        .size:           2
        .value_kind:     hidden_group_size_z
      - .offset:         314
        .size:           2
        .value_kind:     hidden_remainder_x
      - .offset:         316
        .size:           2
        .value_kind:     hidden_remainder_y
      - .offset:         318
        .size:           2
        .value_kind:     hidden_remainder_z
      - .offset:         336
        .size:           8
        .value_kind:     hidden_global_offset_x
      - .offset:         344
        .size:           8
        .value_kind:     hidden_global_offset_y
      - .offset:         352
        .size:           8
        .value_kind:     hidden_global_offset_z
      - .offset:         360
        .size:           2
        .value_kind:     hidden_grid_dims
      - .offset:         416
        .size:           4
        .value_kind:     hidden_dynamic_lds_size
    .group_segment_fixed_size: 0
    .kernarg_segment_align: 8
    .kernarg_segment_size: 552
    .language:       OpenCL C
    .language_version:
      - 2
      - 0
    .max_flat_workgroup_size: 512
    .name:           _Z10hybrid_fwd4Args
    .private_segment_fixed_size: 0
    .sgpr_count:     108
    .sgpr_spill_count: 194
    .symbol:         _Z10hybrid_fwd4Args.kd
    .uniform_work_group_size: 1
    .uses_dynamic_stack: false
    .vgpr_count:     248
    .vgpr_spill_count: 0
    .wavefront_size: 64
